# GEMM1 q/k epilogue: rotary-table loads hoisted and flat loads/stores converted to global with counted waits (a row group no longer waits for the previous group's stores)
# baseline (speedup 1.0000x reference)
; __device__ __forceinline__ unsigned cvt_pk_bf16(float lo, float hi) { unsigned r; asm volatile("v_cvt_pk_bf16_f32 %0, %1, %2" : "=v"(r) : "v"(lo), "v"(hi)); return r; }
;     __device__ __forceinline__ void operator()(const f32x4 (&acc)[2][2][4][2], const Unit& u, int wr, int wc, int fr, int fq) const {
;     ...
;         if (pn < 4) {
;             const bool isq = pn < 2; unsigned char* base = wb + (isq ? OFF_Q : OFF_K) + (unsigned)((pn & 1) * 256 + cl) * 2u;
;             const unsigned char* cs = wb + OFF_ROPE; const unsigned char* sn = cs + 4096 * 32 * 4; const float sc = isq ? qscale : 1.f;
;             const int i0 = 16 * (wc & 1) + 4 * fq;
;             float ks[2][8];
; #pragma unroll
;             for (int bj = 0; bj < 2; ++bj)
; #pragma unroll
;                 for (int e = 0; e < 8; ++e) ks[bj][e] = 0.f;
; #pragma unroll
;             for (int ai = 0; ai < 2; ++ai)
; #pragma unroll
;                 for (int m = 0; m < 4; ++m) {
;                     const int row = row0 + ai * HALF + m * 16, pos = row & 4095;
;                     const unsigned ro = (unsigned)(pos * 32 + i0) * 4u; const f32x4 c4 = *(const f32x4*)(cs + ro), s4 = *(const f32x4*)(sn + ro);
; #pragma unroll
;                     for (int bj = 0; bj < 2; ++bj) {
;                         const f32x4 v0 = acc[ai][bj][m][0], v1 = acc[ai][bj][m][1];
;                         float o[8];
;                         o[0] = v0[0] * c4[0] - v0[1] * s4[0]; o[1] = v0[1] * c4[0] + v0[0] * s4[0];
;                         o[2] = v0[2] * c4[1] - v0[3] * s4[1]; o[3] = v0[3] * c4[1] + v0[2] * s4[1];
;                         o[4] = v1[0] * c4[2] - v1[1] * s4[2]; o[5] = v1[1] * c4[2] + v1[0] * s4[2];
;                         o[6] = v1[2] * c4[3] - v1[3] * s4[3]; o[7] = v1[3] * c4[3] + v1[2] * s4[3];
;                         if (!isq) {
; #pragma unroll
;                             for (int e = 0; e < 8; ++e) ks[bj][e] += o[e]; }
;                         u32x4 w; w.x = cvt_pk_bf16(o[0] * sc, o[1] * sc); w.y = cvt_pk_bf16(o[2] * sc, o[3] * sc); w.z = cvt_pk_bf16(o[4] * sc, o[5] * sc); w.w = cvt_pk_bf16(o[6] * sc, o[7] * sc);
.LBB0_133:
	s_andn2_b64 vcc, exec, s[8:9]
	s_cbranch_vccnz .LBB0_172
	s_cmp_lt_i32 s48, 2
	s_cselect_b64 s[8:9], -1, 0
	s_cmp_gt_i32 s48, 1
	s_cselect_b64 s[50:51], -1, 0
	s_add_u32 s52, s46, 0x1880000
	s_addc_u32 s53, s47, 0
	s_add_u32 s54, s46, 0x1800000
	v_lshlrev_b32_e32 v128, 7, v190
	s_addc_u32 s55, s47, 0
	v_and_or_b32 v128, v128, s78, v182
	v_mov_b32_e32 v129, v145
	v_lshl_add_u64 v[130:131], s[54:55], 0, v[128:129]
	v_add_u32_e32 v250, 0x0, v190
	v_lshlrev_b32_e32 v250, 7, v250
	v_and_or_b32 v250, v250, s78, v182
	global_load_dwordx4 v[200:203], v250, s[54:55]
	global_load_dwordx4 v[204:207], v250, s[52:53]
	v_add_u32_e32 v250, 0x10, v190
	v_lshlrev_b32_e32 v250, 7, v250
	v_and_or_b32 v250, v250, s78, v182
	global_load_dwordx4 v[208:211], v250, s[54:55]
	global_load_dwordx4 v[212:215], v250, s[52:53]
	v_add_u32_e32 v250, 0x20, v190
	v_lshlrev_b32_e32 v250, 7, v250
	v_and_or_b32 v250, v250, s78, v182
	global_load_dwordx4 v[216:219], v250, s[54:55]
	global_load_dwordx4 v[220:223], v250, s[52:53]
	v_add_u32_e32 v250, 0x30, v190
	v_lshlrev_b32_e32 v250, 7, v250
	v_and_or_b32 v250, v250, s78, v182
	global_load_dwordx4 v[224:227], v250, s[54:55]
	global_load_dwordx4 v[228:231], v250, s[52:53]
	v_add_u32_e32 v250, 0x80, v190
	v_lshlrev_b32_e32 v250, 7, v250
	v_and_or_b32 v250, v250, s78, v182
	global_load_dwordx4 v[232:235], v250, s[54:55]
	global_load_dwordx4 v[236:239], v250, s[52:53]
	v_add_u32_e32 v250, 0x90, v190
	v_lshlrev_b32_e32 v250, 7, v250
	v_and_or_b32 v250, v250, s78, v182
	global_load_dwordx4 v[240:243], v250, s[54:55]
	global_load_dwordx4 v[244:247], v250, s[52:53]
	v_lshl_add_u64 v[128:129], s[52:53], 0, v[128:129]
	s_and_b64 vcc, exec, s[50:51]
	s_waitcnt vmcnt(10) lgkmcnt(0)
	v_mov_b32_e32 v132, v200
	v_mov_b32_e32 v133, v201
	v_mov_b32_e32 v134, v202
	v_mov_b32_e32 v135, v203
	v_mov_b32_e32 v128, v204
	v_mov_b32_e32 v129, v205
	v_mov_b32_e32 v130, v206
	v_mov_b32_e32 v131, v207
	v_add_u32_e32 v250, 0xa0, v190
	v_lshlrev_b32_e32 v250, 7, v250
	v_and_or_b32 v250, v250, s78, v182
	global_load_dwordx4 v[200:203], v250, s[54:55]
	global_load_dwordx4 v[204:207], v250, s[52:53]
	v_pk_mul_f32 v[154:155], v[124:125], v[132:133] op_sel_hi:[1,0]
	v_pk_mul_f32 v[158:159], v[120:121], v[134:135] op_sel_hi:[1,0]
	v_mov_b32_e32 v164, v135
	v_pk_mul_f32 v[156:157], v[126:127], v[132:133] op_sel:[0,1]
	v_mov_b32_e32 v192, v131
	v_pk_fma_f32 v[166:167], v[124:125], v[128:129], v[154:155] op_sel:[0,0,1] op_sel_hi:[1,0,0]
	v_pk_fma_f32 v[170:171], v[124:125], v[128:129], v[154:155] op_sel:[0,0,1] op_sel_hi:[1,0,0] neg_lo:[1,0,0] neg_hi:[1,0,0]
	v_pk_fma_f32 v[124:125], v[120:121], v[130:131], v[158:159] op_sel:[0,0,1] op_sel_hi:[1,0,0]
	v_pk_fma_f32 v[162:163], v[120:121], v[130:131], v[158:159] op_sel:[0,0,1] op_sel_hi:[1,0,0] neg_lo:[1,0,0] neg_hi:[1,0,0]
	v_pk_mul_f32 v[120:121], v[122:123], v[164:165] op_sel_hi:[1,0]
	v_pk_fma_f32 v[160:161], v[126:127], v[128:129], v[156:157] op_sel:[0,1,1] op_sel_hi:[1,1,0]
	v_pk_fma_f32 v[168:169], v[126:127], v[128:129], v[156:157] op_sel:[0,1,1] op_sel_hi:[1,1,0] neg_lo:[1,0,0] neg_hi:[1,0,0]
	v_pk_fma_f32 v[126:127], v[122:123], v[192:193], v[120:121] op_sel:[0,0,1] op_sel_hi:[1,0,0]
	v_pk_fma_f32 v[164:165], v[122:123], v[192:193], v[120:121] op_sel:[0,0,1] op_sel_hi:[1,0,0] neg_lo:[1,0,0] neg_hi:[1,0,0]
	s_cbranch_vccz .LBB0_136
	v_mov_b32_e32 v127, v165
	v_mov_b32_e32 v125, v163
	v_mov_b32_e32 v161, v169
	v_mov_b32_e32 v167, v171
	v_pk_add_f32 v[156:157], v[166:167], 0 op_sel_hi:[1,0]
	v_pk_add_f32 v[154:155], v[160:161], 0 op_sel_hi:[1,0]
	v_pk_add_f32 v[122:123], v[124:125], 0 op_sel_hi:[1,0]
	v_pk_add_f32 v[120:121], v[126:127], 0 op_sel_hi:[1,0]
	s_branch .LBB0_137

; __device__ __forceinline__ unsigned cvt_pk_bf16(float lo, float hi) { unsigned r; asm volatile("v_cvt_pk_bf16_f32 %0, %1, %2" : "=v"(r) : "v"(lo), "v"(hi)); return r; }
;     __device__ __forceinline__ void operator()(const f32x4 (&acc)[2][2][4][2], const Unit& u, int wr, int wc, int fr, int fq) const {
;     ...
;                     const int row = row0 + ai * HALF + m * 16, pos = row & 4095;
;                     const unsigned ro = (unsigned)(pos * 32 + i0) * 4u; const f32x4 c4 = *(const f32x4*)(cs + ro), s4 = *(const f32x4*)(sn + ro);
; #pragma unroll
;                     for (int bj = 0; bj < 2; ++bj) {
;                         const f32x4 v0 = acc[ai][bj][m][0], v1 = acc[ai][bj][m][1];
;                         float o[8];
;                         o[0] = v0[0] * c4[0] - v0[1] * s4[0]; o[1] = v0[1] * c4[0] + v0[0] * s4[0];
;                         o[2] = v0[2] * c4[1] - v0[3] * s4[1]; o[3] = v0[3] * c4[1] + v0[2] * s4[1];
;                         o[4] = v1[0] * c4[2] - v1[1] * s4[2]; o[5] = v1[1] * c4[2] + v1[0] * s4[2];
;                         o[6] = v1[2] * c4[3] - v1[3] * s4[3]; o[7] = v1[3] * c4[3] + v1[2] * s4[3];
;                         if (!isq) {
; #pragma unroll
;                             for (int e = 0; e < 8; ++e) ks[bj][e] += o[e]; }
;                         u32x4 w; w.x = cvt_pk_bf16(o[0] * sc, o[1] * sc); w.y = cvt_pk_bf16(o[2] * sc, o[3] * sc); w.z = cvt_pk_bf16(o[4] * sc, o[5] * sc); w.w = cvt_pk_bf16(o[6] * sc, o[7] * sc);
;                         *(u32x4*)(base + (unsigned)(row * 512 + bj * HALF) * 2u) = w;
.LBB0_137:
	v_cndmask_b32_e64 v167, 1.0, v188, s[8:9]
	v_mul_f32_e32 v125, v167, v171
	v_mul_f32_e32 v127, v167, v166
	v_cvt_pk_bf16_f32 v168, v125, v127
	v_mul_f32_e32 v125, v167, v169
	v_mul_f32_e32 v127, v167, v160
	v_cvt_pk_bf16_f32 v169, v125, v127
	v_mul_f32_e32 v125, v167, v163
	v_mul_f32_e32 v124, v167, v124
	v_mov_b32_e32 v192, v132
	v_mov_b32_e32 v193, v132
	s_and_b64 s[34:35], s[8:9], exec
	v_cvt_pk_bf16_f32 v170, v125, v124
	v_mul_f32_e32 v124, v167, v165
	v_mul_f32_e32 v125, v167, v126
	v_mov_b32_e32 v194, v128
	v_mov_b32_e32 v195, v128
	v_mov_b32_e32 v132, v133
	s_cselect_b32 s27, s79, 0x9000000
	v_cvt_pk_bf16_f32 v171, v124, v125
	v_pk_mul_f32 v[124:125], v[116:117], v[192:193]
	v_mov_b32_e32 v128, v129
	v_mov_b32_e32 v196, v134
	v_mov_b32_e32 v197, v134
	s_add_u32 s34, s46, s27
	v_pk_fma_f32 v[162:163], v[116:117], v[194:195], v[124:125] op_sel:[0,0,1] op_sel_hi:[1,1,0]
	v_pk_fma_f32 v[116:117], v[116:117], v[194:195], v[124:125] op_sel:[0,0,1] op_sel_hi:[1,1,0] neg_lo:[1,0,0] neg_hi:[1,0,0]
	v_pk_mul_f32 v[124:125], v[118:119], v[132:133]
	v_mov_b32_e32 v198, v130
	v_mov_b32_e32 v199, v130
	s_addc_u32 s35, s47, 0
	s_and_b32 s27, s48, 1
	v_pk_fma_f32 v[132:133], v[118:119], v[128:129], v[124:125] op_sel:[0,0,1] op_sel_hi:[1,1,0]
	v_pk_fma_f32 v[164:165], v[118:119], v[128:129], v[124:125] op_sel:[0,0,1] op_sel_hi:[1,1,0] neg_lo:[1,0,0] neg_hi:[1,0,0]
	v_pk_mul_f32 v[124:125], v[112:113], v[196:197]
	v_mov_b32_e32 v134, v135
	v_lshl_or_b32 v158, s27, 9, v181
	v_mov_b32_e32 v159, v145
	v_pk_fma_f32 v[118:119], v[112:113], v[198:199], v[124:125] op_sel:[0,0,1] op_sel_hi:[1,1,0]
	v_pk_fma_f32 v[112:113], v[112:113], v[198:199], v[124:125] op_sel:[0,0,1] op_sel_hi:[1,1,0] neg_lo:[1,0,0] neg_hi:[1,0,0]
	v_mov_b32_e32 v130, v131
	v_lshl_add_u64 v[158:159], s[34:35], 0, v[158:159]
	v_pk_mul_f32 v[124:125], v[114:115], v[134:135]
	v_cndmask_b32_e64 v112, 0, 1, s[50:51]
	v_lshl_add_u64 v[160:161], v[158:159], 0, v[144:145]
	v_pk_fma_f32 v[134:135], v[114:115], v[130:131], v[124:125] op_sel:[0,0,1] op_sel_hi:[1,1,0]
	v_cmp_ne_u32_e64 s[8:9], 1, v112
	s_andn2_b64 vcc, exec, s[50:51]
	v_pk_fma_f32 v[114:115], v[114:115], v[130:131], v[124:125] op_sel:[0,0,1] op_sel_hi:[1,1,0] neg_lo:[1,0,0] neg_hi:[1,0,0]
	global_store_dwordx4 v[160:161], v[168:171], off
	s_cbranch_vccnz .LBB0_139
	v_mov_b32_e32 v135, v115
	v_mov_b32_e32 v119, v113
	v_mov_b32_e32 v133, v165
	v_mov_b32_e32 v163, v117
	v_pk_add_f32 v[130:131], v[162:163], 0 op_sel_hi:[1,0]
	v_pk_add_f32 v[128:129], v[132:133], 0 op_sel_hi:[1,0]
	v_pk_add_f32 v[126:127], v[118:119], 0 op_sel_hi:[1,0]
	v_pk_add_f32 v[124:125], v[134:135], 0 op_sel_hi:[1,0]
	s_branch .LBB0_140

; __device__ __forceinline__ unsigned cvt_pk_bf16(float lo, float hi) { unsigned r; asm volatile("v_cvt_pk_bf16_f32 %0, %1, %2" : "=v"(r) : "v"(lo), "v"(hi)); return r; }
;     __device__ __forceinline__ void operator()(const f32x4 (&acc)[2][2][4][2], const Unit& u, int wr, int wc, int fr, int fq) const {
;     ...
;                     const int row = row0 + ai * HALF + m * 16, pos = row & 4095;
;                     const unsigned ro = (unsigned)(pos * 32 + i0) * 4u; const f32x4 c4 = *(const f32x4*)(cs + ro), s4 = *(const f32x4*)(sn + ro);
; #pragma unroll
;                     for (int bj = 0; bj < 2; ++bj) {
;                         const f32x4 v0 = acc[ai][bj][m][0], v1 = acc[ai][bj][m][1];
;                         float o[8];
;                         o[0] = v0[0] * c4[0] - v0[1] * s4[0]; o[1] = v0[1] * c4[0] + v0[0] * s4[0];
;                         o[2] = v0[2] * c4[1] - v0[3] * s4[1]; o[3] = v0[3] * c4[1] + v0[2] * s4[1];
;                         o[4] = v1[0] * c4[2] - v1[1] * s4[2]; o[5] = v1[1] * c4[2] + v1[0] * s4[2];
;                         o[6] = v1[2] * c4[3] - v1[3] * s4[3]; o[7] = v1[3] * c4[3] + v1[2] * s4[3];
;                         if (!isq) {
; #pragma unroll
;                             for (int e = 0; e < 8; ++e) ks[bj][e] += o[e]; }
;                         u32x4 w; w.x = cvt_pk_bf16(o[0] * sc, o[1] * sc); w.y = cvt_pk_bf16(o[2] * sc, o[3] * sc); w.z = cvt_pk_bf16(o[4] * sc, o[5] * sc); w.w = cvt_pk_bf16(o[6] * sc, o[7] * sc);
;                         *(u32x4*)(base + (unsigned)(row * 512 + bj * HALF) * 2u) = w;
.LBB0_140:
	v_mul_f32_e32 v112, v167, v117
	v_mul_f32_e32 v114, v167, v162
	v_cvt_pk_bf16_f32 v168, v112, v114
	v_mul_f32_e32 v112, v167, v165
	v_mul_f32_e32 v114, v167, v132
	v_cvt_pk_bf16_f32 v169, v112, v114
	v_mul_f32_e32 v112, v167, v113
	v_mul_f32_e32 v113, v167, v118
	v_cvt_pk_bf16_f32 v170, v112, v113
	v_mul_f32_e32 v112, v167, v115
	v_add_u32_e32 v164, 16, v190
	v_mul_f32_e32 v113, v167, v134
	v_cvt_pk_bf16_f32 v171, v112, v113
	v_lshlrev_b32_e32 v112, 7, v164
	v_and_or_b32 v144, v112, s78, v182
	v_lshl_add_u64 v[112:113], s[54:55], 0, v[144:145]
	v_lshl_add_u64 v[116:117], s[52:53], 0, v[144:145]
	s_and_b64 vcc, exec, s[8:9]
	global_store_dwordx4 v[160:161], v[168:171], off offset:256
	s_waitcnt vmcnt(12) lgkmcnt(0)
	v_mov_b32_e32 v112, v208
	v_mov_b32_e32 v113, v209
	v_mov_b32_e32 v114, v210
	v_mov_b32_e32 v115, v211
	v_mov_b32_e32 v116, v212
	v_mov_b32_e32 v117, v213
	v_mov_b32_e32 v118, v214
	v_mov_b32_e32 v119, v215
	v_add_u32_e32 v250, 0xb0, v190
	v_lshlrev_b32_e32 v250, 7, v250
	v_and_or_b32 v250, v250, s78, v182
	global_load_dwordx4 v[208:211], v250, s[54:55]
	global_load_dwordx4 v[212:215], v250, s[52:53]
	v_pk_mul_f32 v[132:133], v[108:109], v[112:113] op_sel_hi:[1,0]
	v_pk_mul_f32 v[160:161], v[110:111], v[112:113] op_sel:[0,1]
	v_pk_mul_f32 v[168:169], v[104:105], v[114:115] op_sel_hi:[1,0]
	v_mov_b32_e32 v144, v115
	v_mov_b32_e32 v166, v119
	v_pk_fma_f32 v[134:135], v[108:109], v[116:117], v[132:133] op_sel:[0,0,1] op_sel_hi:[1,0,0]
	v_pk_fma_f32 v[162:163], v[108:109], v[116:117], v[132:133] op_sel:[0,0,1] op_sel_hi:[1,0,0] neg_lo:[1,0,0] neg_hi:[1,0,0]
	v_pk_fma_f32 v[132:133], v[110:111], v[116:117], v[160:161] op_sel:[0,1,1] op_sel_hi:[1,1,0]
	v_pk_fma_f32 v[160:161], v[110:111], v[116:117], v[160:161] op_sel:[0,1,1] op_sel_hi:[1,1,0] neg_lo:[1,0,0] neg_hi:[1,0,0]
	v_pk_fma_f32 v[108:109], v[104:105], v[118:119], v[168:169] op_sel:[0,0,1] op_sel_hi:[1,0,0]
	v_pk_fma_f32 v[110:111], v[104:105], v[118:119], v[168:169] op_sel:[0,0,1] op_sel_hi:[1,0,0] neg_lo:[1,0,0] neg_hi:[1,0,0]
	v_pk_mul_f32 v[168:169], v[106:107], v[144:145] op_sel_hi:[1,0]
	s_nop 0
	v_pk_fma_f32 v[104:105], v[106:107], v[166:167], v[168:169] op_sel:[0,0,1] op_sel_hi:[1,0,0]
	v_pk_fma_f32 v[106:107], v[106:107], v[166:167], v[168:169] op_sel:[0,0,1] op_sel_hi:[1,0,0] neg_lo:[1,0,0] neg_hi:[1,0,0]
	s_cbranch_vccnz .LBB0_142
	v_mov_b32_e32 v105, v107
	v_mov_b32_e32 v109, v111
	v_mov_b32_e32 v133, v161
	v_mov_b32_e32 v135, v163
	v_pk_add_f32 v[156:157], v[156:157], v[134:135]
	v_pk_add_f32 v[154:155], v[154:155], v[132:133]
	v_pk_add_f32 v[122:123], v[122:123], v[108:109]
	v_pk_add_f32 v[120:121], v[120:121], v[104:105]
.LBB0_142:
	v_mul_f32_e32 v105, v167, v163
	v_mul_f32_e32 v106, v167, v134
	v_cvt_pk_bf16_f32 v160, v105, v106
	v_mul_f32_e32 v105, v167, v161
	v_mov_b32_e32 v168, v112
	v_mov_b32_e32 v169, v112
	v_mov_b32_e32 v112, v113
	v_mov_b32_e32 v192, v114
	v_mov_b32_e32 v193, v114
	v_mov_b32_e32 v114, v115
	v_mul_f32_e32 v106, v167, v132
	v_cvt_pk_bf16_f32 v161, v105, v106
	v_mul_f32_e32 v105, v167, v111
	v_mov_b32_e32 v170, v116
	v_mov_b32_e32 v171, v116
	v_mov_b32_e32 v116, v117
	v_mov_b32_e32 v194, v118
	v_mov_b32_e32 v195, v118
	v_mov_b32_e32 v118, v119
	v_lshlrev_b32_e32 v144, 10, v164
	v_mul_f32_e32 v106, v167, v108
	v_cvt_pk_bf16_f32 v162, v105, v106
	v_mul_f32_e32 v105, v167, v107
	v_mul_f32_e32 v104, v167, v104
	v_pk_mul_f32 v[108:109], v[100:101], v[168:169]
	v_pk_mul_f32 v[110:111], v[102:103], v[112:113]
	v_pk_mul_f32 v[112:113], v[96:97], v[192:193]
	v_pk_mul_f32 v[114:115], v[98:99], v[114:115]
	v_cvt_pk_bf16_f32 v163, v105, v104
	v_lshl_add_u64 v[104:105], v[158:159], 0, v[144:145]
	v_pk_fma_f32 v[106:107], v[100:101], v[170:171], v[108:109] op_sel:[0,0,1] op_sel_hi:[1,1,0]
	v_pk_fma_f32 v[100:101], v[100:101], v[170:171], v[108:109] op_sel:[0,0,1] op_sel_hi:[1,1,0] neg_lo:[1,0,0] neg_hi:[1,0,0]
	v_pk_fma_f32 v[108:109], v[102:103], v[116:117], v[110:111] op_sel:[0,0,1] op_sel_hi:[1,1,0]
	v_pk_fma_f32 v[110:111], v[102:103], v[116:117], v[110:111] op_sel:[0,0,1] op_sel_hi:[1,1,0] neg_lo:[1,0,0] neg_hi:[1,0,0]
	v_pk_fma_f32 v[102:103], v[96:97], v[194:195], v[112:113] op_sel:[0,0,1] op_sel_hi:[1,1,0]
	v_pk_fma_f32 v[96:97], v[96:97], v[194:195], v[112:113] op_sel:[0,0,1] op_sel_hi:[1,1,0] neg_lo:[1,0,0] neg_hi:[1,0,0]
	v_pk_fma_f32 v[112:113], v[98:99], v[118:119], v[114:115] op_sel:[0,0,1] op_sel_hi:[1,1,0]
	s_and_b64 vcc, exec, s[8:9]
	v_pk_fma_f32 v[98:99], v[98:99], v[118:119], v[114:115] op_sel:[0,0,1] op_sel_hi:[1,1,0] neg_lo:[1,0,0] neg_hi:[1,0,0]
	global_store_dwordx4 v[104:105], v[160:163], off
	s_cbranch_vccnz .LBB0_144
	v_mov_b32_e32 v113, v99
	v_mov_b32_e32 v103, v97
	v_mov_b32_e32 v109, v111
	v_mov_b32_e32 v107, v101
	v_pk_add_f32 v[130:131], v[130:131], v[106:107]
	v_pk_add_f32 v[128:129], v[128:129], v[108:109]
	v_pk_add_f32 v[126:127], v[126:127], v[102:103]
	v_pk_add_f32 v[124:125], v[124:125], v[112:113]
; __device__ __forceinline__ unsigned cvt_pk_bf16(float lo, float hi) { unsigned r; asm volatile("v_cvt_pk_bf16_f32 %0, %1, %2" : "=v"(r) : "v"(lo), "v"(hi)); return r; }
;     __device__ __forceinline__ void operator()(const f32x4 (&acc)[2][2][4][2], const Unit& u, int wr, int wc, int fr, int fq) const {
;     ...
;                     const int row = row0 + ai * HALF + m * 16, pos = row & 4095;
;                     const unsigned ro = (unsigned)(pos * 32 + i0) * 4u; const f32x4 c4 = *(const f32x4*)(cs + ro), s4 = *(const f32x4*)(sn + ro);
; #pragma unroll
;                     for (int bj = 0; bj < 2; ++bj) {
;                         const f32x4 v0 = acc[ai][bj][m][0], v1 = acc[ai][bj][m][1];
;                         float o[8];
;                         o[0] = v0[0] * c4[0] - v0[1] * s4[0]; o[1] = v0[1] * c4[0] + v0[0] * s4[0];
;                         o[2] = v0[2] * c4[1] - v0[3] * s4[1]; o[3] = v0[3] * c4[1] + v0[2] * s4[1];
;                         o[4] = v1[0] * c4[2] - v1[1] * s4[2]; o[5] = v1[1] * c4[2] + v1[0] * s4[2];
;                         o[6] = v1[2] * c4[3] - v1[3] * s4[3]; o[7] = v1[3] * c4[3] + v1[2] * s4[3];
;                         if (!isq) {
; #pragma unroll
;                             for (int e = 0; e < 8; ++e) ks[bj][e] += o[e]; }
;                         u32x4 w; w.x = cvt_pk_bf16(o[0] * sc, o[1] * sc); w.y = cvt_pk_bf16(o[2] * sc, o[3] * sc); w.z = cvt_pk_bf16(o[4] * sc, o[5] * sc); w.w = cvt_pk_bf16(o[6] * sc, o[7] * sc);
;                         *(u32x4*)(base + (unsigned)(row * 512 + bj * HALF) * 2u) = w;
.LBB0_144:
	v_mul_f32_e32 v96, v167, v101
	v_mul_f32_e32 v98, v167, v106
	v_cvt_pk_bf16_f32 v106, v96, v98
	v_mul_f32_e32 v96, v167, v111
	v_mul_f32_e32 v98, v167, v108
	v_cvt_pk_bf16_f32 v107, v96, v98
	v_mul_f32_e32 v96, v167, v97
	v_mul_f32_e32 v97, v167, v102
	v_cvt_pk_bf16_f32 v108, v96, v97
	v_mul_f32_e32 v96, v167, v99
	v_mul_f32_e32 v97, v167, v112
	v_add_u32_e32 v112, 32, v190
	v_cvt_pk_bf16_f32 v109, v96, v97
	v_lshlrev_b32_e32 v96, 7, v112
	v_and_or_b32 v144, v96, s78, v182
	v_lshl_add_u64 v[96:97], s[54:55], 0, v[144:145]
	v_lshl_add_u64 v[100:101], s[52:53], 0, v[144:145]
	s_and_b64 vcc, exec, s[8:9]
	global_store_dwordx4 v[104:105], v[106:109], off offset:256
	s_waitcnt vmcnt(14) lgkmcnt(0)
	v_mov_b32_e32 v96, v216
	v_mov_b32_e32 v97, v217
	v_mov_b32_e32 v98, v218
	v_mov_b32_e32 v99, v219
	v_mov_b32_e32 v100, v220
	v_mov_b32_e32 v101, v221
	v_mov_b32_e32 v102, v222
	v_mov_b32_e32 v103, v223
	v_pk_mul_f32 v[104:105], v[92:93], v[96:97] op_sel_hi:[1,0]
	v_pk_mul_f32 v[108:109], v[94:95], v[96:97] op_sel:[0,1]
	v_pk_mul_f32 v[114:115], v[88:89], v[98:99] op_sel_hi:[1,0]
	v_mov_b32_e32 v116, v99
	v_mov_b32_e32 v118, v103
	v_pk_fma_f32 v[106:107], v[92:93], v[100:101], v[104:105] op_sel:[0,0,1] op_sel_hi:[1,0,0]
	v_pk_fma_f32 v[110:111], v[92:93], v[100:101], v[104:105] op_sel:[0,0,1] op_sel_hi:[1,0,0] neg_lo:[1,0,0] neg_hi:[1,0,0]
	v_pk_fma_f32 v[104:105], v[94:95], v[100:101], v[108:109] op_sel:[0,1,1] op_sel_hi:[1,1,0]
	v_pk_fma_f32 v[108:109], v[94:95], v[100:101], v[108:109] op_sel:[0,1,1] op_sel_hi:[1,1,0] neg_lo:[1,0,0] neg_hi:[1,0,0]
	v_pk_fma_f32 v[92:93], v[88:89], v[102:103], v[114:115] op_sel:[0,0,1] op_sel_hi:[1,0,0]
	v_pk_fma_f32 v[94:95], v[88:89], v[102:103], v[114:115] op_sel:[0,0,1] op_sel_hi:[1,0,0] neg_lo:[1,0,0] neg_hi:[1,0,0]
	v_pk_mul_f32 v[114:115], v[90:91], v[116:117] op_sel_hi:[1,0]
	s_nop 0
	v_pk_fma_f32 v[88:89], v[90:91], v[118:119], v[114:115] op_sel:[0,0,1] op_sel_hi:[1,0,0]
	v_pk_fma_f32 v[90:91], v[90:91], v[118:119], v[114:115] op_sel:[0,0,1] op_sel_hi:[1,0,0] neg_lo:[1,0,0] neg_hi:[1,0,0]
	s_cbranch_vccnz .LBB0_146
	v_mov_b32_e32 v89, v91
	v_mov_b32_e32 v93, v95
	v_mov_b32_e32 v105, v109
	v_mov_b32_e32 v107, v111
	v_pk_add_f32 v[156:157], v[156:157], v[106:107]
	v_pk_add_f32 v[154:155], v[154:155], v[104:105]
	v_pk_add_f32 v[122:123], v[122:123], v[92:93]
	v_pk_add_f32 v[120:121], v[120:121], v[88:89]
.LBB0_146:
	v_mul_f32_e32 v89, v167, v111
	v_mul_f32_e32 v90, v167, v106
	v_cvt_pk_bf16_f32 v106, v89, v90
	v_mul_f32_e32 v89, v167, v109
	v_mov_b32_e32 v114, v96
	v_mov_b32_e32 v115, v96
	v_mov_b32_e32 v96, v97
	v_mov_b32_e32 v118, v98
	v_mov_b32_e32 v119, v98
	v_mov_b32_e32 v98, v99
	v_mul_f32_e32 v90, v167, v104
	v_cvt_pk_bf16_f32 v107, v89, v90
	v_mul_f32_e32 v89, v167, v95
	v_mov_b32_e32 v116, v100
	v_mov_b32_e32 v117, v100
	v_mov_b32_e32 v100, v101
	v_mov_b32_e32 v132, v102
	v_mov_b32_e32 v133, v102
	v_mov_b32_e32 v102, v103
	v_lshlrev_b32_e32 v144, 10, v112
	v_mul_f32_e32 v90, v167, v92
	v_cvt_pk_bf16_f32 v108, v89, v90
	v_mul_f32_e32 v89, v167, v91
	v_mul_f32_e32 v88, v167, v88
	v_pk_mul_f32 v[92:93], v[84:85], v[114:115]
	v_pk_mul_f32 v[94:95], v[86:87], v[96:97]
	v_pk_mul_f32 v[96:97], v[80:81], v[118:119]
	v_pk_mul_f32 v[98:99], v[82:83], v[98:99]
	v_cvt_pk_bf16_f32 v109, v89, v88
	v_lshl_add_u64 v[88:89], v[158:159], 0, v[144:145]
	v_pk_fma_f32 v[90:91], v[84:85], v[116:117], v[92:93] op_sel:[0,0,1] op_sel_hi:[1,1,0]
	v_pk_fma_f32 v[84:85], v[84:85], v[116:117], v[92:93] op_sel:[0,0,1] op_sel_hi:[1,1,0] neg_lo:[1,0,0] neg_hi:[1,0,0]
	v_pk_fma_f32 v[92:93], v[86:87], v[100:101], v[94:95] op_sel:[0,0,1] op_sel_hi:[1,1,0]
	v_pk_fma_f32 v[94:95], v[86:87], v[100:101], v[94:95] op_sel:[0,0,1] op_sel_hi:[1,1,0] neg_lo:[1,0,0] neg_hi:[1,0,0]
	v_pk_fma_f32 v[86:87], v[80:81], v[132:133], v[96:97] op_sel:[0,0,1] op_sel_hi:[1,1,0]
	v_pk_fma_f32 v[80:81], v[80:81], v[132:133], v[96:97] op_sel:[0,0,1] op_sel_hi:[1,1,0] neg_lo:[1,0,0] neg_hi:[1,0,0]
	v_pk_fma_f32 v[96:97], v[82:83], v[102:103], v[98:99] op_sel:[0,0,1] op_sel_hi:[1,1,0]
	s_and_b64 vcc, exec, s[8:9]
	v_pk_fma_f32 v[82:83], v[82:83], v[102:103], v[98:99] op_sel:[0,0,1] op_sel_hi:[1,1,0] neg_lo:[1,0,0] neg_hi:[1,0,0]
	global_store_dwordx4 v[88:89], v[106:109], off
	s_cbranch_vccnz .LBB0_148
	v_mov_b32_e32 v97, v83
	v_mov_b32_e32 v87, v81
	v_mov_b32_e32 v93, v95
	v_mov_b32_e32 v91, v85
	v_pk_add_f32 v[130:131], v[130:131], v[90:91]
	v_pk_add_f32 v[128:129], v[128:129], v[92:93]
	v_pk_add_f32 v[126:127], v[126:127], v[86:87]
	v_pk_add_f32 v[124:125], v[124:125], v[96:97]
; __device__ __forceinline__ unsigned cvt_pk_bf16(float lo, float hi) { unsigned r; asm volatile("v_cvt_pk_bf16_f32 %0, %1, %2" : "=v"(r) : "v"(lo), "v"(hi)); return r; }
;     __device__ __forceinline__ void operator()(const f32x4 (&acc)[2][2][4][2], const Unit& u, int wr, int wc, int fr, int fq) const {
;     ...
;                     const int row = row0 + ai * HALF + m * 16, pos = row & 4095;
;                     const unsigned ro = (unsigned)(pos * 32 + i0) * 4u; const f32x4 c4 = *(const f32x4*)(cs + ro), s4 = *(const f32x4*)(sn + ro);
; #pragma unroll
;                     for (int bj = 0; bj < 2; ++bj) {
;                         const f32x4 v0 = acc[ai][bj][m][0], v1 = acc[ai][bj][m][1];
;                         float o[8];
;                         o[0] = v0[0] * c4[0] - v0[1] * s4[0]; o[1] = v0[1] * c4[0] + v0[0] * s4[0];
;                         o[2] = v0[2] * c4[1] - v0[3] * s4[1]; o[3] = v0[3] * c4[1] + v0[2] * s4[1];
;                         o[4] = v1[0] * c4[2] - v1[1] * s4[2]; o[5] = v1[1] * c4[2] + v1[0] * s4[2];
;                         o[6] = v1[2] * c4[3] - v1[3] * s4[3]; o[7] = v1[3] * c4[3] + v1[2] * s4[3];
;                         if (!isq) {
; #pragma unroll
;                             for (int e = 0; e < 8; ++e) ks[bj][e] += o[e]; }
;                         u32x4 w; w.x = cvt_pk_bf16(o[0] * sc, o[1] * sc); w.y = cvt_pk_bf16(o[2] * sc, o[3] * sc); w.z = cvt_pk_bf16(o[4] * sc, o[5] * sc); w.w = cvt_pk_bf16(o[6] * sc, o[7] * sc);
;                         *(u32x4*)(base + (unsigned)(row * 512 + bj * HALF) * 2u) = w;
.LBB0_148:
	v_mul_f32_e32 v80, v167, v85
	v_mul_f32_e32 v82, v167, v90
	v_cvt_pk_bf16_f32 v90, v80, v82
	v_mul_f32_e32 v80, v167, v95
	v_mul_f32_e32 v82, v167, v92
	v_cvt_pk_bf16_f32 v91, v80, v82
	v_mul_f32_e32 v80, v167, v81
	v_mul_f32_e32 v81, v167, v86
	v_cvt_pk_bf16_f32 v92, v80, v81
	v_mul_f32_e32 v80, v167, v83
	v_mul_f32_e32 v81, v167, v96
	v_add_u32_e32 v96, 48, v190
	v_cvt_pk_bf16_f32 v93, v80, v81
	v_lshlrev_b32_e32 v80, 7, v96
	v_and_or_b32 v144, v80, s78, v182
	v_lshl_add_u64 v[80:81], s[54:55], 0, v[144:145]
	v_lshl_add_u64 v[84:85], s[52:53], 0, v[144:145]
	s_and_b64 vcc, exec, s[8:9]
	global_store_dwordx4 v[88:89], v[90:93], off offset:256
	s_waitcnt vmcnt(14) lgkmcnt(0)
	v_mov_b32_e32 v80, v224
	v_mov_b32_e32 v81, v225
	v_mov_b32_e32 v82, v226
	v_mov_b32_e32 v83, v227
	v_mov_b32_e32 v84, v228
	v_mov_b32_e32 v85, v229
	v_mov_b32_e32 v86, v230
	v_mov_b32_e32 v87, v231
	v_pk_mul_f32 v[88:89], v[76:77], v[80:81] op_sel_hi:[1,0]
	v_pk_mul_f32 v[92:93], v[78:79], v[80:81] op_sel:[0,1]
	v_pk_mul_f32 v[98:99], v[72:73], v[82:83] op_sel_hi:[1,0]
	v_mov_b32_e32 v100, v83
	v_mov_b32_e32 v102, v87
	v_pk_fma_f32 v[90:91], v[76:77], v[84:85], v[88:89] op_sel:[0,0,1] op_sel_hi:[1,0,0]
	v_pk_fma_f32 v[94:95], v[76:77], v[84:85], v[88:89] op_sel:[0,0,1] op_sel_hi:[1,0,0] neg_lo:[1,0,0] neg_hi:[1,0,0]
	v_pk_fma_f32 v[88:89], v[78:79], v[84:85], v[92:93] op_sel:[0,1,1] op_sel_hi:[1,1,0]
	v_pk_fma_f32 v[92:93], v[78:79], v[84:85], v[92:93] op_sel:[0,1,1] op_sel_hi:[1,1,0] neg_lo:[1,0,0] neg_hi:[1,0,0]
	v_pk_fma_f32 v[76:77], v[72:73], v[86:87], v[98:99] op_sel:[0,0,1] op_sel_hi:[1,0,0]
	v_pk_fma_f32 v[78:79], v[72:73], v[86:87], v[98:99] op_sel:[0,0,1] op_sel_hi:[1,0,0] neg_lo:[1,0,0] neg_hi:[1,0,0]
	v_pk_mul_f32 v[98:99], v[74:75], v[100:101] op_sel_hi:[1,0]
	s_nop 0
	v_pk_fma_f32 v[72:73], v[74:75], v[102:103], v[98:99] op_sel:[0,0,1] op_sel_hi:[1,0,0]
	v_pk_fma_f32 v[74:75], v[74:75], v[102:103], v[98:99] op_sel:[0,0,1] op_sel_hi:[1,0,0] neg_lo:[1,0,0] neg_hi:[1,0,0]
	s_cbranch_vccnz .LBB0_150
	v_mov_b32_e32 v73, v75
	v_mov_b32_e32 v77, v79
	v_mov_b32_e32 v89, v93
	v_mov_b32_e32 v91, v95
	v_pk_add_f32 v[156:157], v[156:157], v[90:91]
	v_pk_add_f32 v[154:155], v[154:155], v[88:89]
	v_pk_add_f32 v[122:123], v[122:123], v[76:77]
	v_pk_add_f32 v[120:121], v[120:121], v[72:73]
.LBB0_150:
	v_mul_f32_e32 v73, v167, v95
	v_mul_f32_e32 v74, v167, v90
	v_cvt_pk_bf16_f32 v90, v73, v74
	v_mul_f32_e32 v73, v167, v93
	v_mov_b32_e32 v98, v80
	v_mov_b32_e32 v99, v80
	v_mov_b32_e32 v80, v81
	v_mov_b32_e32 v102, v82
	v_mov_b32_e32 v103, v82
	v_mov_b32_e32 v82, v83
	v_mul_f32_e32 v74, v167, v88
	v_cvt_pk_bf16_f32 v91, v73, v74
	v_mul_f32_e32 v73, v167, v79
	v_mov_b32_e32 v100, v84
	v_mov_b32_e32 v101, v84
	v_mov_b32_e32 v84, v85
	v_mov_b32_e32 v104, v86
	v_mov_b32_e32 v105, v86
	v_mov_b32_e32 v86, v87
	v_lshlrev_b32_e32 v144, 10, v96
	v_mul_f32_e32 v74, v167, v76
	v_cvt_pk_bf16_f32 v92, v73, v74
	v_mul_f32_e32 v73, v167, v75
	v_mul_f32_e32 v72, v167, v72
	v_pk_mul_f32 v[76:77], v[68:69], v[98:99]
	v_pk_mul_f32 v[78:79], v[70:71], v[80:81]
	v_pk_mul_f32 v[80:81], v[64:65], v[102:103]
	v_pk_mul_f32 v[82:83], v[66:67], v[82:83]
	v_cvt_pk_bf16_f32 v93, v73, v72
	v_lshl_add_u64 v[72:73], v[158:159], 0, v[144:145]
	v_pk_fma_f32 v[74:75], v[68:69], v[100:101], v[76:77] op_sel:[0,0,1] op_sel_hi:[1,1,0]
	v_pk_fma_f32 v[68:69], v[68:69], v[100:101], v[76:77] op_sel:[0,0,1] op_sel_hi:[1,1,0] neg_lo:[1,0,0] neg_hi:[1,0,0]
	v_pk_fma_f32 v[76:77], v[70:71], v[84:85], v[78:79] op_sel:[0,0,1] op_sel_hi:[1,1,0]
	v_pk_fma_f32 v[78:79], v[70:71], v[84:85], v[78:79] op_sel:[0,0,1] op_sel_hi:[1,1,0] neg_lo:[1,0,0] neg_hi:[1,0,0]
	v_pk_fma_f32 v[70:71], v[64:65], v[104:105], v[80:81] op_sel:[0,0,1] op_sel_hi:[1,1,0]
	v_pk_fma_f32 v[64:65], v[64:65], v[104:105], v[80:81] op_sel:[0,0,1] op_sel_hi:[1,1,0] neg_lo:[1,0,0] neg_hi:[1,0,0]
	v_pk_fma_f32 v[80:81], v[66:67], v[86:87], v[82:83] op_sel:[0,0,1] op_sel_hi:[1,1,0]
	s_and_b64 vcc, exec, s[8:9]
	v_pk_fma_f32 v[66:67], v[66:67], v[86:87], v[82:83] op_sel:[0,0,1] op_sel_hi:[1,1,0] neg_lo:[1,0,0] neg_hi:[1,0,0]
	global_store_dwordx4 v[72:73], v[90:93], off
	s_cbranch_vccnz .LBB0_152
	v_mov_b32_e32 v81, v67
	v_mov_b32_e32 v71, v65
	v_mov_b32_e32 v77, v79
	v_mov_b32_e32 v75, v69
	v_pk_add_f32 v[130:131], v[130:131], v[74:75]
	v_pk_add_f32 v[128:129], v[128:129], v[76:77]
	v_pk_add_f32 v[126:127], v[126:127], v[70:71]
	v_pk_add_f32 v[124:125], v[124:125], v[80:81]
.LBB0_152:
	v_mul_f32_e32 v64, v167, v69
	v_mul_f32_e32 v66, v167, v74
	v_cvt_pk_bf16_f32 v74, v64, v66
	v_mul_f32_e32 v64, v167, v79
	v_mul_f32_e32 v66, v167, v76
	v_cvt_pk_bf16_f32 v75, v64, v66
	v_mul_f32_e32 v64, v167, v65
	v_mul_f32_e32 v65, v167, v70
	v_cvt_pk_bf16_f32 v76, v64, v65
	v_mul_f32_e32 v64, v167, v67
	v_mul_f32_e32 v65, v167, v80
	v_add_u32_e32 v80, 0x80, v190
	v_cvt_pk_bf16_f32 v77, v64, v65
	v_lshlrev_b32_e32 v64, 7, v80
	v_and_or_b32 v144, v64, s78, v182
	v_lshl_add_u64 v[64:65], s[54:55], 0, v[144:145]
	v_lshl_add_u64 v[68:69], s[52:53], 0, v[144:145]
	s_and_b64 vcc, exec, s[8:9]
	global_store_dwordx4 v[72:73], v[74:77], off offset:256
	s_waitcnt vmcnt(14) lgkmcnt(0)
	v_mov_b32_e32 v64, v232
	v_mov_b32_e32 v65, v233
	v_mov_b32_e32 v66, v234
	v_mov_b32_e32 v67, v235
	v_mov_b32_e32 v68, v236
	v_mov_b32_e32 v69, v237
	v_mov_b32_e32 v70, v238
	v_mov_b32_e32 v71, v239
	v_pk_mul_f32 v[72:73], v[60:61], v[64:65] op_sel_hi:[1,0]
	v_pk_mul_f32 v[76:77], v[62:63], v[64:65] op_sel:[0,1]
	v_pk_mul_f32 v[82:83], v[56:57], v[66:67] op_sel_hi:[1,0]
	v_mov_b32_e32 v84, v67
	v_mov_b32_e32 v86, v71
	v_pk_fma_f32 v[74:75], v[60:61], v[68:69], v[72:73] op_sel:[0,0,1] op_sel_hi:[1,0,0]
	v_pk_fma_f32 v[78:79], v[60:61], v[68:69], v[72:73] op_sel:[0,0,1] op_sel_hi:[1,0,0] neg_lo:[1,0,0] neg_hi:[1,0,0]
	v_pk_fma_f32 v[72:73], v[62:63], v[68:69], v[76:77] op_sel:[0,1,1] op_sel_hi:[1,1,0]
	v_pk_fma_f32 v[76:77], v[62:63], v[68:69], v[76:77] op_sel:[0,1,1] op_sel_hi:[1,1,0] neg_lo:[1,0,0] neg_hi:[1,0,0]
	v_pk_fma_f32 v[60:61], v[56:57], v[70:71], v[82:83] op_sel:[0,0,1] op_sel_hi:[1,0,0]
	v_pk_fma_f32 v[62:63], v[56:57], v[70:71], v[82:83] op_sel:[0,0,1] op_sel_hi:[1,0,0] neg_lo:[1,0,0] neg_hi:[1,0,0]
	v_pk_mul_f32 v[82:83], v[58:59], v[84:85] op_sel_hi:[1,0]
	s_nop 0
	v_pk_fma_f32 v[56:57], v[58:59], v[86:87], v[82:83] op_sel:[0,0,1] op_sel_hi:[1,0,0]
	v_pk_fma_f32 v[58:59], v[58:59], v[86:87], v[82:83] op_sel:[0,0,1] op_sel_hi:[1,0,0] neg_lo:[1,0,0] neg_hi:[1,0,0]
	s_cbranch_vccnz .LBB0_154
	v_mov_b32_e32 v57, v59
	v_mov_b32_e32 v61, v63
	v_mov_b32_e32 v73, v77
	v_mov_b32_e32 v75, v79
	v_pk_add_f32 v[156:157], v[156:157], v[74:75]
	v_pk_add_f32 v[154:155], v[154:155], v[72:73]
	v_pk_add_f32 v[122:123], v[122:123], v[60:61]
	v_pk_add_f32 v[120:121], v[120:121], v[56:57]
; __device__ __forceinline__ unsigned cvt_pk_bf16(float lo, float hi) { unsigned r; asm volatile("v_cvt_pk_bf16_f32 %0, %1, %2" : "=v"(r) : "v"(lo), "v"(hi)); return r; }
;     __device__ __forceinline__ void operator()(const f32x4 (&acc)[2][2][4][2], const Unit& u, int wr, int wc, int fr, int fq) const {
;     ...
;                     const int row = row0 + ai * HALF + m * 16, pos = row & 4095;
;                     const unsigned ro = (unsigned)(pos * 32 + i0) * 4u; const f32x4 c4 = *(const f32x4*)(cs + ro), s4 = *(const f32x4*)(sn + ro);
; #pragma unroll
;                     for (int bj = 0; bj < 2; ++bj) {
;                         const f32x4 v0 = acc[ai][bj][m][0], v1 = acc[ai][bj][m][1];
;                         float o[8];
;                         o[0] = v0[0] * c4[0] - v0[1] * s4[0]; o[1] = v0[1] * c4[0] + v0[0] * s4[0];
;                         o[2] = v0[2] * c4[1] - v0[3] * s4[1]; o[3] = v0[3] * c4[1] + v0[2] * s4[1];
;                         o[4] = v1[0] * c4[2] - v1[1] * s4[2]; o[5] = v1[1] * c4[2] + v1[0] * s4[2];
;                         o[6] = v1[2] * c4[3] - v1[3] * s4[3]; o[7] = v1[3] * c4[3] + v1[2] * s4[3];
;                         if (!isq) {
; #pragma unroll
;                             for (int e = 0; e < 8; ++e) ks[bj][e] += o[e]; }
;                         u32x4 w; w.x = cvt_pk_bf16(o[0] * sc, o[1] * sc); w.y = cvt_pk_bf16(o[2] * sc, o[3] * sc); w.z = cvt_pk_bf16(o[4] * sc, o[5] * sc); w.w = cvt_pk_bf16(o[6] * sc, o[7] * sc);
;                         *(u32x4*)(base + (unsigned)(row * 512 + bj * HALF) * 2u) = w;
.LBB0_154:
	v_mul_f32_e32 v57, v167, v79
	v_mul_f32_e32 v58, v167, v74
	v_cvt_pk_bf16_f32 v74, v57, v58
	v_mul_f32_e32 v57, v167, v77
	v_mov_b32_e32 v82, v64
	v_mov_b32_e32 v83, v64
	v_mov_b32_e32 v64, v65
	v_mov_b32_e32 v86, v66
	v_mov_b32_e32 v87, v66
	v_mov_b32_e32 v66, v67
	v_mul_f32_e32 v58, v167, v72
	v_cvt_pk_bf16_f32 v75, v57, v58
	v_mul_f32_e32 v57, v167, v63
	v_mov_b32_e32 v84, v68
	v_mov_b32_e32 v85, v68
	v_mov_b32_e32 v68, v69
	v_mov_b32_e32 v88, v70
	v_mov_b32_e32 v89, v70
	v_mov_b32_e32 v70, v71
	v_lshlrev_b32_e32 v144, 10, v80
	v_mul_f32_e32 v58, v167, v60
	v_cvt_pk_bf16_f32 v76, v57, v58
	v_mul_f32_e32 v57, v167, v59
	v_mul_f32_e32 v56, v167, v56
	v_pk_mul_f32 v[60:61], v[52:53], v[82:83]
	v_pk_mul_f32 v[62:63], v[54:55], v[64:65]
	v_pk_mul_f32 v[64:65], v[48:49], v[86:87]
	v_pk_mul_f32 v[66:67], v[50:51], v[66:67]
	v_cvt_pk_bf16_f32 v77, v57, v56
	v_lshl_add_u64 v[56:57], v[158:159], 0, v[144:145]
	v_pk_fma_f32 v[58:59], v[52:53], v[84:85], v[60:61] op_sel:[0,0,1] op_sel_hi:[1,1,0]
	v_pk_fma_f32 v[52:53], v[52:53], v[84:85], v[60:61] op_sel:[0,0,1] op_sel_hi:[1,1,0] neg_lo:[1,0,0] neg_hi:[1,0,0]
	v_pk_fma_f32 v[60:61], v[54:55], v[68:69], v[62:63] op_sel:[0,0,1] op_sel_hi:[1,1,0]
	v_pk_fma_f32 v[62:63], v[54:55], v[68:69], v[62:63] op_sel:[0,0,1] op_sel_hi:[1,1,0] neg_lo:[1,0,0] neg_hi:[1,0,0]
	v_pk_fma_f32 v[54:55], v[48:49], v[88:89], v[64:65] op_sel:[0,0,1] op_sel_hi:[1,1,0]
	v_pk_fma_f32 v[48:49], v[48:49], v[88:89], v[64:65] op_sel:[0,0,1] op_sel_hi:[1,1,0] neg_lo:[1,0,0] neg_hi:[1,0,0]
	v_pk_fma_f32 v[64:65], v[50:51], v[70:71], v[66:67] op_sel:[0,0,1] op_sel_hi:[1,1,0]
	s_and_b64 vcc, exec, s[8:9]
	v_pk_fma_f32 v[50:51], v[50:51], v[70:71], v[66:67] op_sel:[0,0,1] op_sel_hi:[1,1,0] neg_lo:[1,0,0] neg_hi:[1,0,0]
	global_store_dwordx4 v[56:57], v[74:77], off
	s_cbranch_vccnz .LBB0_156
	v_mov_b32_e32 v65, v51
	v_mov_b32_e32 v55, v49
	v_mov_b32_e32 v61, v63
	v_mov_b32_e32 v59, v53
	v_pk_add_f32 v[130:131], v[130:131], v[58:59]
	v_pk_add_f32 v[128:129], v[128:129], v[60:61]
	v_pk_add_f32 v[126:127], v[126:127], v[54:55]
	v_pk_add_f32 v[124:125], v[124:125], v[64:65]
.LBB0_156:
	v_mul_f32_e32 v48, v167, v53
	v_mul_f32_e32 v50, v167, v58
	v_cvt_pk_bf16_f32 v58, v48, v50
	v_mul_f32_e32 v48, v167, v63
	v_mul_f32_e32 v50, v167, v60
	v_cvt_pk_bf16_f32 v59, v48, v50
	v_mul_f32_e32 v48, v167, v49
	v_mul_f32_e32 v49, v167, v54
	v_cvt_pk_bf16_f32 v60, v48, v49
	v_mul_f32_e32 v48, v167, v51
	v_mul_f32_e32 v49, v167, v64
	v_add_u32_e32 v64, 0x90, v190
	v_cvt_pk_bf16_f32 v61, v48, v49
	v_lshlrev_b32_e32 v48, 7, v64
	v_and_or_b32 v144, v48, s78, v182
	v_lshl_add_u64 v[48:49], s[54:55], 0, v[144:145]
	v_lshl_add_u64 v[52:53], s[52:53], 0, v[144:145]
	s_and_b64 vcc, exec, s[8:9]
	global_store_dwordx4 v[56:57], v[58:61], off offset:256
	s_waitcnt vmcnt(14) lgkmcnt(0)
	v_mov_b32_e32 v48, v240
	v_mov_b32_e32 v49, v241
	v_mov_b32_e32 v50, v242
	v_mov_b32_e32 v51, v243
	v_mov_b32_e32 v52, v244
	v_mov_b32_e32 v53, v245
	v_mov_b32_e32 v54, v246
	v_mov_b32_e32 v55, v247
	v_pk_mul_f32 v[56:57], v[44:45], v[48:49] op_sel_hi:[1,0]
	v_pk_mul_f32 v[60:61], v[46:47], v[48:49] op_sel:[0,1]
	v_pk_mul_f32 v[66:67], v[40:41], v[50:51] op_sel_hi:[1,0]
	v_mov_b32_e32 v68, v51
	v_mov_b32_e32 v70, v55
	v_pk_fma_f32 v[58:59], v[44:45], v[52:53], v[56:57] op_sel:[0,0,1] op_sel_hi:[1,0,0]
	v_pk_fma_f32 v[62:63], v[44:45], v[52:53], v[56:57] op_sel:[0,0,1] op_sel_hi:[1,0,0] neg_lo:[1,0,0] neg_hi:[1,0,0]
	v_pk_fma_f32 v[56:57], v[46:47], v[52:53], v[60:61] op_sel:[0,1,1] op_sel_hi:[1,1,0]
	v_pk_fma_f32 v[60:61], v[46:47], v[52:53], v[60:61] op_sel:[0,1,1] op_sel_hi:[1,1,0] neg_lo:[1,0,0] neg_hi:[1,0,0]
	v_pk_fma_f32 v[44:45], v[40:41], v[54:55], v[66:67] op_sel:[0,0,1] op_sel_hi:[1,0,0]
	v_pk_fma_f32 v[46:47], v[40:41], v[54:55], v[66:67] op_sel:[0,0,1] op_sel_hi:[1,0,0] neg_lo:[1,0,0] neg_hi:[1,0,0]
	v_pk_mul_f32 v[66:67], v[42:43], v[68:69] op_sel_hi:[1,0]
	s_nop 0
	v_pk_fma_f32 v[40:41], v[42:43], v[70:71], v[66:67] op_sel:[0,0,1] op_sel_hi:[1,0,0]
	v_pk_fma_f32 v[42:43], v[42:43], v[70:71], v[66:67] op_sel:[0,0,1] op_sel_hi:[1,0,0] neg_lo:[1,0,0] neg_hi:[1,0,0]
	s_cbranch_vccnz .LBB0_158
	v_mov_b32_e32 v41, v43
	v_mov_b32_e32 v45, v47
	v_mov_b32_e32 v57, v61
	v_mov_b32_e32 v59, v63
	v_pk_add_f32 v[156:157], v[156:157], v[58:59]
	v_pk_add_f32 v[154:155], v[154:155], v[56:57]
	v_pk_add_f32 v[122:123], v[122:123], v[44:45]
	v_pk_add_f32 v[120:121], v[120:121], v[40:41]
.LBB0_158:
	v_mul_f32_e32 v41, v167, v63
	v_mul_f32_e32 v42, v167, v58
	v_cvt_pk_bf16_f32 v58, v41, v42
	v_mul_f32_e32 v41, v167, v61
	v_mov_b32_e32 v66, v48
	v_mov_b32_e32 v67, v48
	v_mov_b32_e32 v48, v49
	v_mov_b32_e32 v70, v50
	v_mov_b32_e32 v71, v50
	v_mov_b32_e32 v50, v51
	v_mul_f32_e32 v42, v167, v56
	v_cvt_pk_bf16_f32 v59, v41, v42
	v_mul_f32_e32 v41, v167, v47
	v_mov_b32_e32 v68, v52
	v_mov_b32_e32 v69, v52
	v_mov_b32_e32 v52, v53
	v_mov_b32_e32 v72, v54
	v_mov_b32_e32 v73, v54
	v_mov_b32_e32 v54, v55
	v_lshlrev_b32_e32 v144, 10, v64
	v_mul_f32_e32 v42, v167, v44
	v_cvt_pk_bf16_f32 v60, v41, v42
	v_mul_f32_e32 v41, v167, v43
	v_mul_f32_e32 v40, v167, v40
	v_pk_mul_f32 v[44:45], v[36:37], v[66:67]
	v_pk_mul_f32 v[46:47], v[38:39], v[48:49]
	v_pk_mul_f32 v[48:49], v[32:33], v[70:71]
	v_pk_mul_f32 v[50:51], v[34:35], v[50:51]
	v_cvt_pk_bf16_f32 v61, v41, v40
	v_lshl_add_u64 v[40:41], v[158:159], 0, v[144:145]
	v_pk_fma_f32 v[42:43], v[36:37], v[68:69], v[44:45] op_sel:[0,0,1] op_sel_hi:[1,1,0]
	v_pk_fma_f32 v[36:37], v[36:37], v[68:69], v[44:45] op_sel:[0,0,1] op_sel_hi:[1,1,0] neg_lo:[1,0,0] neg_hi:[1,0,0]
	v_pk_fma_f32 v[44:45], v[38:39], v[52:53], v[46:47] op_sel:[0,0,1] op_sel_hi:[1,1,0]
	v_pk_fma_f32 v[46:47], v[38:39], v[52:53], v[46:47] op_sel:[0,0,1] op_sel_hi:[1,1,0] neg_lo:[1,0,0] neg_hi:[1,0,0]
	v_pk_fma_f32 v[38:39], v[32:33], v[72:73], v[48:49] op_sel:[0,0,1] op_sel_hi:[1,1,0]
	v_pk_fma_f32 v[32:33], v[32:33], v[72:73], v[48:49] op_sel:[0,0,1] op_sel_hi:[1,1,0] neg_lo:[1,0,0] neg_hi:[1,0,0]
	v_pk_fma_f32 v[48:49], v[34:35], v[54:55], v[50:51] op_sel:[0,0,1] op_sel_hi:[1,1,0]
	s_and_b64 vcc, exec, s[8:9]
	v_pk_fma_f32 v[34:35], v[34:35], v[54:55], v[50:51] op_sel:[0,0,1] op_sel_hi:[1,1,0] neg_lo:[1,0,0] neg_hi:[1,0,0]
	global_store_dwordx4 v[40:41], v[58:61], off
	s_cbranch_vccnz .LBB0_160
	v_mov_b32_e32 v49, v35
	v_mov_b32_e32 v39, v33
	v_mov_b32_e32 v45, v47
	v_mov_b32_e32 v43, v37
	v_pk_add_f32 v[130:131], v[130:131], v[42:43]
	v_pk_add_f32 v[128:129], v[128:129], v[44:45]
	v_pk_add_f32 v[126:127], v[126:127], v[38:39]
	v_pk_add_f32 v[124:125], v[124:125], v[48:49]
; __device__ __forceinline__ unsigned cvt_pk_bf16(float lo, float hi) { unsigned r; asm volatile("v_cvt_pk_bf16_f32 %0, %1, %2" : "=v"(r) : "v"(lo), "v"(hi)); return r; }
;     __device__ __forceinline__ void operator()(const f32x4 (&acc)[2][2][4][2], const Unit& u, int wr, int wc, int fr, int fq) const {
;     ...
;                     const int row = row0 + ai * HALF + m * 16, pos = row & 4095;
;                     const unsigned ro = (unsigned)(pos * 32 + i0) * 4u; const f32x4 c4 = *(const f32x4*)(cs + ro), s4 = *(const f32x4*)(sn + ro);
; #pragma unroll
;                     for (int bj = 0; bj < 2; ++bj) {
;                         const f32x4 v0 = acc[ai][bj][m][0], v1 = acc[ai][bj][m][1];
;                         float o[8];
;                         o[0] = v0[0] * c4[0] - v0[1] * s4[0]; o[1] = v0[1] * c4[0] + v0[0] * s4[0];
;                         o[2] = v0[2] * c4[1] - v0[3] * s4[1]; o[3] = v0[3] * c4[1] + v0[2] * s4[1];
;                         o[4] = v1[0] * c4[2] - v1[1] * s4[2]; o[5] = v1[1] * c4[2] + v1[0] * s4[2];
;                         o[6] = v1[2] * c4[3] - v1[3] * s4[3]; o[7] = v1[3] * c4[3] + v1[2] * s4[3];
;                         if (!isq) {
; #pragma unroll
;                             for (int e = 0; e < 8; ++e) ks[bj][e] += o[e]; }
;                         u32x4 w; w.x = cvt_pk_bf16(o[0] * sc, o[1] * sc); w.y = cvt_pk_bf16(o[2] * sc, o[3] * sc); w.z = cvt_pk_bf16(o[4] * sc, o[5] * sc); w.w = cvt_pk_bf16(o[6] * sc, o[7] * sc);
;                         *(u32x4*)(base + (unsigned)(row * 512 + bj * HALF) * 2u) = w;
.LBB0_160:
	v_mul_f32_e32 v32, v167, v37
	v_mul_f32_e32 v34, v167, v42
	v_cvt_pk_bf16_f32 v42, v32, v34
	v_mul_f32_e32 v32, v167, v47
	v_mul_f32_e32 v34, v167, v44
	v_cvt_pk_bf16_f32 v43, v32, v34
	v_mul_f32_e32 v32, v167, v33
	v_mul_f32_e32 v33, v167, v38
	v_cvt_pk_bf16_f32 v44, v32, v33
	v_mul_f32_e32 v32, v167, v35
	v_mul_f32_e32 v33, v167, v48
	v_add_u32_e32 v48, 0xa0, v190
	v_cvt_pk_bf16_f32 v45, v32, v33
	v_lshlrev_b32_e32 v32, 7, v48
	v_and_or_b32 v144, v32, s78, v182
	v_lshl_add_u64 v[32:33], s[54:55], 0, v[144:145]
	v_lshl_add_u64 v[36:37], s[52:53], 0, v[144:145]
	s_and_b64 vcc, exec, s[8:9]
	global_store_dwordx4 v[40:41], v[42:45], off offset:256
	s_waitcnt vmcnt(14) lgkmcnt(0)
	v_mov_b32_e32 v32, v200
	v_mov_b32_e32 v33, v201
	v_mov_b32_e32 v34, v202
	v_mov_b32_e32 v35, v203
	v_mov_b32_e32 v36, v204
	v_mov_b32_e32 v37, v205
	v_mov_b32_e32 v38, v206
	v_mov_b32_e32 v39, v207
	v_pk_mul_f32 v[40:41], v[28:29], v[32:33] op_sel_hi:[1,0]
	v_pk_mul_f32 v[44:45], v[30:31], v[32:33] op_sel:[0,1]
	v_pk_mul_f32 v[50:51], v[24:25], v[34:35] op_sel_hi:[1,0]
	v_mov_b32_e32 v52, v35
	v_mov_b32_e32 v54, v39
	v_pk_fma_f32 v[42:43], v[28:29], v[36:37], v[40:41] op_sel:[0,0,1] op_sel_hi:[1,0,0]
	v_pk_fma_f32 v[46:47], v[28:29], v[36:37], v[40:41] op_sel:[0,0,1] op_sel_hi:[1,0,0] neg_lo:[1,0,0] neg_hi:[1,0,0]
	v_pk_fma_f32 v[40:41], v[30:31], v[36:37], v[44:45] op_sel:[0,1,1] op_sel_hi:[1,1,0]
	v_pk_fma_f32 v[44:45], v[30:31], v[36:37], v[44:45] op_sel:[0,1,1] op_sel_hi:[1,1,0] neg_lo:[1,0,0] neg_hi:[1,0,0]
	v_pk_fma_f32 v[28:29], v[24:25], v[38:39], v[50:51] op_sel:[0,0,1] op_sel_hi:[1,0,0]
	v_pk_fma_f32 v[30:31], v[24:25], v[38:39], v[50:51] op_sel:[0,0,1] op_sel_hi:[1,0,0] neg_lo:[1,0,0] neg_hi:[1,0,0]
	v_pk_mul_f32 v[50:51], v[26:27], v[52:53] op_sel_hi:[1,0]
	s_nop 0
	v_pk_fma_f32 v[24:25], v[26:27], v[54:55], v[50:51] op_sel:[0,0,1] op_sel_hi:[1,0,0]
	v_pk_fma_f32 v[26:27], v[26:27], v[54:55], v[50:51] op_sel:[0,0,1] op_sel_hi:[1,0,0] neg_lo:[1,0,0] neg_hi:[1,0,0]
	s_cbranch_vccnz .LBB0_162
	v_mov_b32_e32 v25, v27
	v_mov_b32_e32 v29, v31
	v_mov_b32_e32 v41, v45
	v_mov_b32_e32 v43, v47
	v_pk_add_f32 v[156:157], v[156:157], v[42:43]
	v_pk_add_f32 v[154:155], v[154:155], v[40:41]
	v_pk_add_f32 v[122:123], v[122:123], v[28:29]
	v_pk_add_f32 v[120:121], v[120:121], v[24:25]
.LBB0_162:
	v_mul_f32_e32 v25, v167, v47
	v_mul_f32_e32 v26, v167, v42
	v_cvt_pk_bf16_f32 v42, v25, v26
	v_mul_f32_e32 v25, v167, v45
	v_mov_b32_e32 v50, v32
	v_mov_b32_e32 v51, v32
	v_mov_b32_e32 v32, v33
	v_mov_b32_e32 v54, v34
	v_mov_b32_e32 v55, v34
	v_mov_b32_e32 v34, v35
	v_mul_f32_e32 v26, v167, v40
	v_cvt_pk_bf16_f32 v43, v25, v26
	v_mul_f32_e32 v25, v167, v31
	v_mov_b32_e32 v52, v36
	v_mov_b32_e32 v53, v36
	v_mov_b32_e32 v36, v37
	v_mov_b32_e32 v56, v38
	v_mov_b32_e32 v57, v38
	v_mov_b32_e32 v38, v39
	v_lshlrev_b32_e32 v144, 10, v48
	v_mul_f32_e32 v26, v167, v28
	v_cvt_pk_bf16_f32 v44, v25, v26
	v_mul_f32_e32 v25, v167, v27
	v_mul_f32_e32 v24, v167, v24
	v_pk_mul_f32 v[28:29], v[20:21], v[50:51]
	v_pk_mul_f32 v[30:31], v[22:23], v[32:33]
	v_pk_mul_f32 v[32:33], v[16:17], v[54:55]
	v_pk_mul_f32 v[34:35], v[18:19], v[34:35]
	v_cvt_pk_bf16_f32 v45, v25, v24
	v_lshl_add_u64 v[24:25], v[158:159], 0, v[144:145]
	v_pk_fma_f32 v[26:27], v[20:21], v[52:53], v[28:29] op_sel:[0,0,1] op_sel_hi:[1,1,0]
	v_pk_fma_f32 v[20:21], v[20:21], v[52:53], v[28:29] op_sel:[0,0,1] op_sel_hi:[1,1,0] neg_lo:[1,0,0] neg_hi:[1,0,0]
	v_pk_fma_f32 v[28:29], v[22:23], v[36:37], v[30:31] op_sel:[0,0,1] op_sel_hi:[1,1,0]
	v_pk_fma_f32 v[30:31], v[22:23], v[36:37], v[30:31] op_sel:[0,0,1] op_sel_hi:[1,1,0] neg_lo:[1,0,0] neg_hi:[1,0,0]
	v_pk_fma_f32 v[22:23], v[16:17], v[56:57], v[32:33] op_sel:[0,0,1] op_sel_hi:[1,1,0]
	v_pk_fma_f32 v[16:17], v[16:17], v[56:57], v[32:33] op_sel:[0,0,1] op_sel_hi:[1,1,0] neg_lo:[1,0,0] neg_hi:[1,0,0]
	v_pk_fma_f32 v[32:33], v[18:19], v[38:39], v[34:35] op_sel:[0,0,1] op_sel_hi:[1,1,0]
	s_and_b64 vcc, exec, s[8:9]
	v_pk_fma_f32 v[18:19], v[18:19], v[38:39], v[34:35] op_sel:[0,0,1] op_sel_hi:[1,1,0] neg_lo:[1,0,0] neg_hi:[1,0,0]
	global_store_dwordx4 v[24:25], v[42:45], off
	s_cbranch_vccnz .LBB0_164
	v_mov_b32_e32 v33, v19
	v_mov_b32_e32 v23, v17
	v_mov_b32_e32 v29, v31
	v_mov_b32_e32 v27, v21
	v_pk_add_f32 v[130:131], v[130:131], v[26:27]
	v_pk_add_f32 v[128:129], v[128:129], v[28:29]
	v_pk_add_f32 v[126:127], v[126:127], v[22:23]
	v_pk_add_f32 v[124:125], v[124:125], v[32:33]
.LBB0_164:
	v_mul_f32_e32 v16, v167, v21
	v_mul_f32_e32 v18, v167, v26
	v_cvt_pk_bf16_f32 v26, v16, v18
	v_mul_f32_e32 v16, v167, v31
	v_mul_f32_e32 v18, v167, v28
	v_cvt_pk_bf16_f32 v27, v16, v18
	v_mul_f32_e32 v16, v167, v17
	v_mul_f32_e32 v17, v167, v22
	v_cvt_pk_bf16_f32 v28, v16, v17
	v_mul_f32_e32 v16, v167, v19
	v_mul_f32_e32 v17, v167, v32
	v_add_u32_e32 v32, 0xb0, v190
	v_cvt_pk_bf16_f32 v29, v16, v17
	v_lshlrev_b32_e32 v16, 7, v32
	v_and_or_b32 v144, v16, s78, v182
	v_lshl_add_u64 v[16:17], s[54:55], 0, v[144:145]
	v_lshl_add_u64 v[20:21], s[52:53], 0, v[144:145]
	s_and_b64 vcc, exec, s[8:9]
	global_store_dwordx4 v[24:25], v[26:29], off offset:256
	s_waitcnt vmcnt(12) lgkmcnt(0)
	v_mov_b32_e32 v16, v208
	v_mov_b32_e32 v17, v209
	v_mov_b32_e32 v18, v210
	v_mov_b32_e32 v19, v211
	v_mov_b32_e32 v20, v212
	v_mov_b32_e32 v21, v213
	v_mov_b32_e32 v22, v214
	v_mov_b32_e32 v23, v215
	v_pk_mul_f32 v[24:25], v[12:13], v[16:17] op_sel_hi:[1,0]
	v_pk_mul_f32 v[28:29], v[14:15], v[16:17] op_sel:[0,1]
	v_pk_mul_f32 v[34:35], v[8:9], v[18:19] op_sel_hi:[1,0]
	v_mov_b32_e32 v36, v19
	v_mov_b32_e32 v38, v23
	v_pk_fma_f32 v[26:27], v[12:13], v[20:21], v[24:25] op_sel:[0,0,1] op_sel_hi:[1,0,0]
	v_pk_fma_f32 v[30:31], v[12:13], v[20:21], v[24:25] op_sel:[0,0,1] op_sel_hi:[1,0,0] neg_lo:[1,0,0] neg_hi:[1,0,0]
	v_pk_fma_f32 v[24:25], v[14:15], v[20:21], v[28:29] op_sel:[0,1,1] op_sel_hi:[1,1,0]
	v_pk_fma_f32 v[28:29], v[14:15], v[20:21], v[28:29] op_sel:[0,1,1] op_sel_hi:[1,1,0] neg_lo:[1,0,0] neg_hi:[1,0,0]
	v_pk_fma_f32 v[12:13], v[8:9], v[22:23], v[34:35] op_sel:[0,0,1] op_sel_hi:[1,0,0]
	v_pk_fma_f32 v[14:15], v[8:9], v[22:23], v[34:35] op_sel:[0,0,1] op_sel_hi:[1,0,0] neg_lo:[1,0,0] neg_hi:[1,0,0]
	v_pk_mul_f32 v[34:35], v[10:11], v[36:37] op_sel_hi:[1,0]
	s_nop 0
	v_pk_fma_f32 v[8:9], v[10:11], v[38:39], v[34:35] op_sel:[0,0,1] op_sel_hi:[1,0,0]
	v_pk_fma_f32 v[10:11], v[10:11], v[38:39], v[34:35] op_sel:[0,0,1] op_sel_hi:[1,0,0] neg_lo:[1,0,0] neg_hi:[1,0,0]
	s_cbranch_vccnz .LBB0_166
	v_mov_b32_e32 v9, v11
	v_mov_b32_e32 v13, v15
	v_mov_b32_e32 v25, v29
	v_mov_b32_e32 v27, v31
	v_pk_add_f32 v[156:157], v[156:157], v[26:27]
	v_pk_add_f32 v[154:155], v[154:155], v[24:25]
	v_pk_add_f32 v[122:123], v[122:123], v[12:13]
	v_pk_add_f32 v[120:121], v[120:121], v[8:9]
; __device__ __forceinline__ unsigned cvt_pk_bf16(float lo, float hi) { unsigned r; asm volatile("v_cvt_pk_bf16_f32 %0, %1, %2" : "=v"(r) : "v"(lo), "v"(hi)); return r; }
;     __device__ __forceinline__ void operator()(const f32x4 (&acc)[2][2][4][2], const Unit& u, int wr, int wc, int fr, int fq) const {
;     ...
;                     const int row = row0 + ai * HALF + m * 16, pos = row & 4095;
;                     const unsigned ro = (unsigned)(pos * 32 + i0) * 4u; const f32x4 c4 = *(const f32x4*)(cs + ro), s4 = *(const f32x4*)(sn + ro);
; #pragma unroll
;                     for (int bj = 0; bj < 2; ++bj) {
;                         const f32x4 v0 = acc[ai][bj][m][0], v1 = acc[ai][bj][m][1];
;                         float o[8];
;                         o[0] = v0[0] * c4[0] - v0[1] * s4[0]; o[1] = v0[1] * c4[0] + v0[0] * s4[0];
;                         o[2] = v0[2] * c4[1] - v0[3] * s4[1]; o[3] = v0[3] * c4[1] + v0[2] * s4[1];
;                         o[4] = v1[0] * c4[2] - v1[1] * s4[2]; o[5] = v1[1] * c4[2] + v1[0] * s4[2];
;                         o[6] = v1[2] * c4[3] - v1[3] * s4[3]; o[7] = v1[3] * c4[3] + v1[2] * s4[3];
;                         if (!isq) {
; #pragma unroll
;                             for (int e = 0; e < 8; ++e) ks[bj][e] += o[e]; }
;                         u32x4 w; w.x = cvt_pk_bf16(o[0] * sc, o[1] * sc); w.y = cvt_pk_bf16(o[2] * sc, o[3] * sc); w.z = cvt_pk_bf16(o[4] * sc, o[5] * sc); w.w = cvt_pk_bf16(o[6] * sc, o[7] * sc);
;                         *(u32x4*)(base + (unsigned)(row * 512 + bj * HALF) * 2u) = w;
.LBB0_166:
	v_mul_f32_e32 v9, v167, v31
	v_mul_f32_e32 v10, v167, v26
	v_cvt_pk_bf16_f32 v26, v9, v10
	v_mul_f32_e32 v9, v167, v29
	v_mov_b32_e32 v34, v16
	v_mov_b32_e32 v35, v16
	v_mov_b32_e32 v16, v17
	v_mov_b32_e32 v38, v18
	v_mov_b32_e32 v39, v18
	v_mov_b32_e32 v18, v19
	v_mul_f32_e32 v10, v167, v24
	v_cvt_pk_bf16_f32 v27, v9, v10
	v_mul_f32_e32 v9, v167, v15
	v_mov_b32_e32 v36, v20
	v_mov_b32_e32 v37, v20
	v_mov_b32_e32 v20, v21
	v_mov_b32_e32 v40, v22
	v_mov_b32_e32 v41, v22
	v_mov_b32_e32 v22, v23
	v_lshlrev_b32_e32 v144, 10, v32
	v_mul_f32_e32 v10, v167, v12
	v_cvt_pk_bf16_f32 v28, v9, v10
	v_mul_f32_e32 v9, v167, v11
	v_mul_f32_e32 v8, v167, v8
	v_pk_mul_f32 v[12:13], v[4:5], v[34:35]
	v_pk_mul_f32 v[14:15], v[6:7], v[16:17]
	v_pk_mul_f32 v[16:17], v[0:1], v[38:39]
	v_pk_mul_f32 v[18:19], v[2:3], v[18:19]
	v_cvt_pk_bf16_f32 v29, v9, v8
	v_lshl_add_u64 v[8:9], v[158:159], 0, v[144:145]
	v_pk_fma_f32 v[10:11], v[4:5], v[36:37], v[12:13] op_sel:[0,0,1] op_sel_hi:[1,1,0]
	v_pk_fma_f32 v[4:5], v[4:5], v[36:37], v[12:13] op_sel:[0,0,1] op_sel_hi:[1,1,0] neg_lo:[1,0,0] neg_hi:[1,0,0]
	v_pk_fma_f32 v[12:13], v[6:7], v[20:21], v[14:15] op_sel:[0,0,1] op_sel_hi:[1,1,0]
	v_pk_fma_f32 v[14:15], v[6:7], v[20:21], v[14:15] op_sel:[0,0,1] op_sel_hi:[1,1,0] neg_lo:[1,0,0] neg_hi:[1,0,0]
	v_pk_fma_f32 v[6:7], v[0:1], v[40:41], v[16:17] op_sel:[0,0,1] op_sel_hi:[1,1,0]
	v_pk_fma_f32 v[0:1], v[0:1], v[40:41], v[16:17] op_sel:[0,0,1] op_sel_hi:[1,1,0] neg_lo:[1,0,0] neg_hi:[1,0,0]
	v_pk_fma_f32 v[16:17], v[2:3], v[22:23], v[18:19] op_sel:[0,0,1] op_sel_hi:[1,1,0]
	s_and_b64 vcc, exec, s[8:9]
	v_pk_fma_f32 v[2:3], v[2:3], v[22:23], v[18:19] op_sel:[0,0,1] op_sel_hi:[1,1,0] neg_lo:[1,0,0] neg_hi:[1,0,0]
	global_store_dwordx4 v[8:9], v[26:29], off
	s_cbranch_vccnz .LBB0_168
	v_mov_b32_e32 v17, v3
	v_mov_b32_e32 v7, v1
	v_mov_b32_e32 v13, v15
	v_mov_b32_e32 v11, v5
	v_pk_add_f32 v[130:131], v[130:131], v[10:11]
	v_pk_add_f32 v[128:129], v[128:129], v[12:13]
	v_pk_add_f32 v[126:127], v[126:127], v[6:7]
	v_pk_add_f32 v[124:125], v[124:125], v[16:17]
;     __device__ __forceinline__ void operator()(const f32x4 (&acc)[2][2][4][2], const Unit& u, int wr, int wc, int fr, int fq) const {
;     ...
;                         *(u32x4*)(base + (unsigned)(row * 512 + bj * HALF) * 2u) = w;
;                     }
;                 }
;             if (!isq) {
; #pragma unroll
;                 for (int bj = 0; bj < 2; ++bj)
; #pragma unroll
;                     for (int e = 0; e < 8; ++e) { float s = ks[bj][e]; s += __shfl_xor(s, 1); s += __shfl_xor(s, 2); s += __shfl_xor(s, 4); s += __shfl_xor(s, 8); ks[bj][e] = s; }
;                 if (fr == 0 && do_km) {
;                     const int b = u.pm >> 4, nb = u.pm & 15;
; #pragma unroll
;                     for (int bj = 0; bj < 2; ++bj) { const int h = (pn & 1) * 4 + 2 * bj + (wc >> 1); float* kp = (float*)(wb + OFF_KMEAN + (unsigned)(layer * 32768 + ((b * 8 + h) * 16 + nb) * 64 + 32 * (wc & 1) + 8 * fq) * 4u);
; #pragma unroll
;                         for (int e = 0; e < 8; ++e) unsafeAtomicAdd(kp + e, ks[bj][e] * (1.0f / 256.0f)); }
.LBB0_168:
	v_mul_f32_e32 v0, v167, v5
	v_mul_f32_e32 v2, v167, v10
	v_cvt_pk_bf16_f32 v4, v0, v2
	v_mul_f32_e32 v0, v167, v15
	v_mul_f32_e32 v2, v167, v12
	v_cvt_pk_bf16_f32 v5, v0, v2
	v_mul_f32_e32 v0, v167, v1
	v_mul_f32_e32 v1, v167, v6
	s_and_b64 vcc, exec, s[50:51]
	v_cvt_pk_bf16_f32 v6, v0, v1
	v_mul_f32_e32 v0, v167, v3
	v_mul_f32_e32 v1, v167, v16
	v_cvt_pk_bf16_f32 v7, v0, v1
	global_store_dwordx4 v[8:9], v[4:7], off offset:256
	s_cbranch_vccz .LBB0_172
	ds_bpermute_b32 v1, v173, v156
	ds_bpermute_b32 v2, v173, v155
	ds_bpermute_b32 v5, v173, v154
	ds_bpermute_b32 v8, v173, v123
	ds_bpermute_b32 v11, v173, v122
	s_waitcnt lgkmcnt(0)
	v_add_f32_e32 v1, v156, v1
	ds_bpermute_b32 v4, v174, v1
	v_add_f32_e32 v6, v155, v2
	v_add_f32_e32 v8, v123, v8
	ds_bpermute_b32 v10, v174, v8
	ds_bpermute_b32 v18, v173, v130
	s_waitcnt lgkmcnt(0)
	v_add_f32_e32 v1, v1, v4
	v_add_f32_e32 v4, v154, v5
	ds_bpermute_b32 v5, v174, v6
	ds_bpermute_b32 v7, v174, v4
	v_add_f32_e32 v8, v8, v10
	v_add_f32_e32 v11, v122, v11
	ds_bpermute_b32 v10, v175, v8
	s_waitcnt lgkmcnt(0)
	v_add_f32_e32 v5, v6, v5
	v_add_f32_e32 v7, v4, v7
	ds_bpermute_b32 v6, v175, v5
	ds_bpermute_b32 v9, v175, v7
	ds_bpermute_b32 v12, v174, v11
	v_add_f32_e32 v18, v130, v18
	ds_bpermute_b32 v20, v174, v18
	s_waitcnt lgkmcnt(0)
	v_add_f32_e32 v4, v5, v6
	v_add_f32_e32 v6, v7, v9
	ds_bpermute_b32 v9, v173, v121
	ds_bpermute_b32 v21, v173, v129
	v_add_f32_e32 v8, v8, v10
	v_add_f32_e32 v10, v11, v12
	ds_bpermute_b32 v15, v173, v131
	s_waitcnt lgkmcnt(0)
	v_add_f32_e32 v13, v121, v9
	ds_bpermute_b32 v14, v174, v13
	v_add_f32_e32 v18, v18, v20
	v_add_f32_e32 v20, v129, v21
	v_add_f32_e32 v15, v131, v15
	ds_bpermute_b32 v21, v174, v20
	s_waitcnt lgkmcnt(0)
	v_add_f32_e32 v12, v13, v14
	ds_bpermute_b32 v14, v173, v120
	ds_bpermute_b32 v22, v173, v128
	ds_bpermute_b32 v17, v174, v15
	v_add_f32_e32 v20, v20, v21
	ds_bpermute_b32 v0, v173, v157
	s_waitcnt lgkmcnt(0)
	v_add_f32_e32 v14, v120, v14
	ds_bpermute_b32 v16, v174, v14
	v_add_f32_e32 v21, v128, v22
	v_add_f32_e32 v17, v15, v17
	ds_bpermute_b32 v22, v174, v21
	ds_bpermute_b32 v19, v175, v17
	s_waitcnt lgkmcnt(0)
	v_add_f32_e32 v14, v14, v16
	ds_bpermute_b32 v16, v175, v14
	ds_bpermute_b32 v27, v173, v125
	v_add_f32_e32 v22, v21, v22
	ds_bpermute_b32 v26, v175, v22
	ds_bpermute_b32 v28, v173, v124
	s_waitcnt lgkmcnt(0)
	v_add_f32_e32 v14, v14, v16
	v_add_f32_e32 v16, v17, v19
	ds_bpermute_b32 v19, v175, v18
	v_add_f32_e32 v22, v22, v26
	ds_bpermute_b32 v26, v173, v126
	v_add_f32_e32 v0, v157, v0
	v_add_f32_e32 v27, v125, v27
	s_waitcnt lgkmcnt(0)
	v_add_f32_e32 v18, v18, v19
	ds_bpermute_b32 v19, v173, v127
	v_add_f32_e32 v26, v126, v26
	v_add_f32_e32 v28, v124, v28
	ds_bpermute_b32 v3, v174, v0
	ds_bpermute_b32 v29, v174, v26
	s_waitcnt lgkmcnt(0)
	v_add_f32_e32 v24, v127, v19
	ds_bpermute_b32 v25, v174, v24
	ds_bpermute_b32 v30, v174, v27
	ds_bpermute_b32 v31, v174, v28
	v_add_f32_e32 v0, v0, v3
	v_add_f32_e32 v26, v26, v29
	s_waitcnt lgkmcnt(0)
	v_add_f32_e32 v24, v24, v25
	v_add_f32_e32 v30, v27, v30
	v_add_f32_e32 v31, v28, v31
	ds_bpermute_b32 v2, v175, v0
	ds_bpermute_b32 v3, v175, v1
	ds_bpermute_b32 v11, v175, v10
	ds_bpermute_b32 v13, v175, v12
	ds_bpermute_b32 v23, v175, v20
	ds_bpermute_b32 v25, v175, v24
	ds_bpermute_b32 v29, v175, v26
	ds_bpermute_b32 v32, v175, v30
	ds_bpermute_b32 v33, v175, v31
	s_waitcnt lgkmcnt(0)
	v_add_f32_e32 v0, v0, v2
	v_add_f32_e32 v2, v1, v3
	v_add_f32_e32 v10, v10, v11
	v_add_f32_e32 v12, v12, v13
	v_add_f32_e32 v20, v20, v23
	v_add_f32_e32 v24, v24, v25
	v_add_f32_e32 v26, v26, v29
	v_add_f32_e32 v28, v30, v32
	v_add_f32_e32 v30, v31, v33
	ds_bpermute_b32 v1, v176, v0
	ds_bpermute_b32 v3, v176, v2
	ds_bpermute_b32 v5, v176, v4
	ds_bpermute_b32 v7, v176, v6
	ds_bpermute_b32 v9, v176, v8
	ds_bpermute_b32 v11, v176, v10
	ds_bpermute_b32 v13, v176, v12
	ds_bpermute_b32 v15, v176, v14
	ds_bpermute_b32 v17, v176, v16
	ds_bpermute_b32 v19, v176, v18
	ds_bpermute_b32 v21, v176, v20
	ds_bpermute_b32 v23, v176, v22
	ds_bpermute_b32 v25, v176, v24
	ds_bpermute_b32 v27, v176, v26
	ds_bpermute_b32 v29, v176, v28
	ds_bpermute_b32 v31, v176, v30
	s_and_saveexec_b64 s[8:9], s[4:5]
	s_cbranch_execz .LBB0_171
	s_lshl_b32 s27, s27, 2
	s_or_b32 s27, s27, s73
	s_add_u32 s34, s46, 0x80000
	s_addc_u32 s35, s47, 0
	s_lshr_b32 s29, s14, 1
	s_and_b32 s29, s29, 0x3ffff8
	s_lshl_b32 s14, s14, 6
	s_or_b32 s27, s27, s29
	s_and_b32 s14, s14, 0x3c0
	s_or_b32 s14, s14, s74
	s_lshl_b32 s27, s27, 10
	s_or_b32 s29, s14, s27
	s_waitcnt lgkmcnt(0)
	v_add_f32_e32 v2, v2, v3
	v_add_f32_e32 v3, v0, v1
	v_or_b32_e32 v0, s29, v179
	v_lshlrev_b32_e32 v144, 2, v0
	v_lshl_add_u64 v[0:1], s[34:35], 0, v[144:145]
	v_mul_f32_e32 v3, 0x3b800000, v3
	v_add_f32_e32 v4, v4, v5
	flat_atomic_add_f32 v[0:1], v3
	v_mul_f32_e32 v2, 0x3b800000, v2
	v_add_f32_e32 v6, v6, v7
	flat_atomic_add_f32 v[0:1], v2 offset:4
	v_mul_f32_e32 v2, 0x3b800000, v4
	v_add_f32_e32 v8, v8, v9
	flat_atomic_add_f32 v[0:1], v2 offset:8
	v_mul_f32_e32 v2, 0x3b800000, v6
	v_add_f32_e32 v10, v10, v11
	flat_atomic_add_f32 v[0:1], v2 offset:12
	v_mul_f32_e32 v2, 0x3b800000, v8
	v_add_f32_e32 v12, v12, v13
	flat_atomic_add_f32 v[0:1], v2 offset:16
	v_mul_f32_e32 v2, 0x3b800000, v10
	v_add_f32_e32 v14, v14, v15
	flat_atomic_add_f32 v[0:1], v2 offset:20
	v_mul_f32_e32 v2, 0x3b800000, v12
	flat_atomic_add_f32 v[0:1], v2 offset:24
	v_mul_f32_e32 v2, 0x3b800000, v14
	flat_atomic_add_f32 v[0:1], v2 offset:28
	v_or_b32_e32 v0, s14, v179
	v_or_b32_e32 v0, s27, v0
	v_add_f32_e32 v16, v16, v17
	v_lshl_or_b32 v144, v0, 2, v189
	v_add_f32_e32 v18, v18, v19
	v_lshl_add_u64 v[0:1], s[34:35], 0, v[144:145]
	v_mul_f32_e32 v2, 0x3b800000, v16
	v_add_f32_e32 v20, v20, v21
	flat_atomic_add_f32 v[0:1], v2
	v_mul_f32_e32 v2, 0x3b800000, v18
	v_add_f32_e32 v22, v22, v23
	flat_atomic_add_f32 v[0:1], v2 offset:4
	v_mul_f32_e32 v2, 0x3b800000, v20
	v_add_f32_e32 v24, v24, v25
	flat_atomic_add_f32 v[0:1], v2 offset:8
	v_mul_f32_e32 v2, 0x3b800000, v22
	v_add_f32_e32 v26, v26, v27
	flat_atomic_add_f32 v[0:1], v2 offset:12
	v_mul_f32_e32 v2, 0x3b800000, v24
	v_add_f32_e32 v28, v28, v29
	flat_atomic_add_f32 v[0:1], v2 offset:16
	v_mul_f32_e32 v2, 0x3b800000, v26
	v_add_f32_e32 v30, v30, v31
	flat_atomic_add_f32 v[0:1], v2 offset:20
	v_mul_f32_e32 v2, 0x3b800000, v28
	flat_atomic_add_f32 v[0:1], v2 offset:24
	v_mul_f32_e32 v2, 0x3b800000, v30
	flat_atomic_add_f32 v[0:1], v2 offset:28

; __device__ __forceinline__ unsigned cvt_pk_bf16(float lo, float hi) { unsigned r; asm volatile("v_cvt_pk_bf16_f32 %0, %1, %2" : "=v"(r) : "v"(lo), "v"(hi)); return r; }
;     __device__ __forceinline__ void operator()(const f32x4 (&acc)[2][2][4][2], const Unit& u, int wr, int wc, int fr, int fq) const {
;     ...
;         if (pn < 4) {
;             const bool isq = pn < 2; unsigned char* base = wb + (isq ? OFF_Q : OFF_K) + (unsigned)((pn & 1) * 256 + cl) * 2u;
;             const unsigned char* cs = wb + OFF_ROPE; const unsigned char* sn = cs + 4096 * 32 * 4; const float sc = isq ? qscale : 1.f;
;             const int i0 = 16 * (wc & 1) + 4 * fq;
;             float ks[2][8];
; #pragma unroll
;             for (int bj = 0; bj < 2; ++bj)
; #pragma unroll
;                 for (int e = 0; e < 8; ++e) ks[bj][e] = 0.f;
; #pragma unroll
;             for (int ai = 0; ai < 2; ++ai)
; #pragma unroll
;                 for (int m = 0; m < 4; ++m) {
;                     const int row = row0 + ai * HALF + m * 16, pos = row & 4095;
;                     const unsigned ro = (unsigned)(pos * 32 + i0) * 4u; const f32x4 c4 = *(const f32x4*)(cs + ro), s4 = *(const f32x4*)(sn + ro);
; #pragma unroll
;                     for (int bj = 0; bj < 2; ++bj) {
;                         const f32x4 v0 = acc[ai][bj][m][0], v1 = acc[ai][bj][m][1];
;                         float o[8];
;                         o[0] = v0[0] * c4[0] - v0[1] * s4[0]; o[1] = v0[1] * c4[0] + v0[0] * s4[0];
;                         o[2] = v0[2] * c4[1] - v0[3] * s4[1]; o[3] = v0[3] * c4[1] + v0[2] * s4[1];
;                         o[4] = v1[0] * c4[2] - v1[1] * s4[2]; o[5] = v1[1] * c4[2] + v1[0] * s4[2];
;                         o[6] = v1[2] * c4[3] - v1[3] * s4[3]; o[7] = v1[3] * c4[3] + v1[2] * s4[3];
;                         if (!isq) {
; #pragma unroll
;                             for (int e = 0; e < 8; ++e) ks[bj][e] += o[e]; }
;                         u32x4 w; w.x = cvt_pk_bf16(o[0] * sc, o[1] * sc); w.y = cvt_pk_bf16(o[2] * sc, o[3] * sc); w.z = cvt_pk_bf16(o[4] * sc, o[5] * sc); w.w = cvt_pk_bf16(o[6] * sc, o[7] * sc);
.LBB0_1129:
	s_andn2_b64 vcc, exec, s[8:9]
	s_cbranch_vccnz .LBB0_1168
	s_cmp_lt_i32 s48, 2
	s_cselect_b64 s[8:9], -1, 0
	s_cmp_gt_i32 s48, 1
	s_cselect_b64 s[50:51], -1, 0
	s_add_u32 s52, s46, 0x1880000
	s_addc_u32 s53, s47, 0
	s_add_u32 s54, s46, 0x1800000
	v_lshlrev_b32_e32 v128, 7, v191
	s_addc_u32 s55, s47, 0
	v_and_or_b32 v128, v128, s78, v182
	v_mov_b32_e32 v129, v145
	v_lshl_add_u64 v[130:131], s[54:55], 0, v[128:129]
	v_add_u32_e32 v250, 0x0, v191
	v_lshlrev_b32_e32 v250, 7, v250
	v_and_or_b32 v250, v250, s78, v182
	global_load_dwordx4 v[200:203], v250, s[54:55]
	global_load_dwordx4 v[204:207], v250, s[52:53]
	v_add_u32_e32 v250, 0x10, v191
	v_lshlrev_b32_e32 v250, 7, v250
	v_and_or_b32 v250, v250, s78, v182
	global_load_dwordx4 v[208:211], v250, s[54:55]
	global_load_dwordx4 v[212:215], v250, s[52:53]
	v_add_u32_e32 v250, 0x20, v191
	v_lshlrev_b32_e32 v250, 7, v250
	v_and_or_b32 v250, v250, s78, v182
	global_load_dwordx4 v[216:219], v250, s[54:55]
	global_load_dwordx4 v[220:223], v250, s[52:53]
	v_add_u32_e32 v250, 0x30, v191
	v_lshlrev_b32_e32 v250, 7, v250
	v_and_or_b32 v250, v250, s78, v182
	global_load_dwordx4 v[224:227], v250, s[54:55]
	global_load_dwordx4 v[228:231], v250, s[52:53]
	v_add_u32_e32 v250, 0x80, v191
	v_lshlrev_b32_e32 v250, 7, v250
	v_and_or_b32 v250, v250, s78, v182
	global_load_dwordx4 v[232:235], v250, s[54:55]
	global_load_dwordx4 v[236:239], v250, s[52:53]
	v_add_u32_e32 v250, 0x90, v191
	v_lshlrev_b32_e32 v250, 7, v250
	v_and_or_b32 v250, v250, s78, v182
	global_load_dwordx4 v[240:243], v250, s[54:55]
	global_load_dwordx4 v[244:247], v250, s[52:53]
	v_lshl_add_u64 v[128:129], s[52:53], 0, v[128:129]
	s_and_b64 vcc, exec, s[50:51]
	s_waitcnt vmcnt(10) lgkmcnt(0)
	v_mov_b32_e32 v132, v200
	v_mov_b32_e32 v133, v201
	v_mov_b32_e32 v134, v202
	v_mov_b32_e32 v135, v203
	v_mov_b32_e32 v128, v204
	v_mov_b32_e32 v129, v205
	v_mov_b32_e32 v130, v206
	v_mov_b32_e32 v131, v207
	v_add_u32_e32 v250, 0xa0, v191
	v_lshlrev_b32_e32 v250, 7, v250
	v_and_or_b32 v250, v250, s78, v182
	global_load_dwordx4 v[200:203], v250, s[54:55]
	global_load_dwordx4 v[204:207], v250, s[52:53]
	v_pk_mul_f32 v[154:155], v[124:125], v[132:133] op_sel_hi:[1,0]
	v_pk_mul_f32 v[158:159], v[120:121], v[134:135] op_sel_hi:[1,0]
	v_mov_b32_e32 v164, v135
	v_pk_mul_f32 v[156:157], v[126:127], v[132:133] op_sel:[0,1]
	v_mov_b32_e32 v192, v131
	v_pk_fma_f32 v[166:167], v[124:125], v[128:129], v[154:155] op_sel:[0,0,1] op_sel_hi:[1,0,0]
	v_pk_fma_f32 v[170:171], v[124:125], v[128:129], v[154:155] op_sel:[0,0,1] op_sel_hi:[1,0,0] neg_lo:[1,0,0] neg_hi:[1,0,0]
	v_pk_fma_f32 v[124:125], v[120:121], v[130:131], v[158:159] op_sel:[0,0,1] op_sel_hi:[1,0,0]
	v_pk_fma_f32 v[162:163], v[120:121], v[130:131], v[158:159] op_sel:[0,0,1] op_sel_hi:[1,0,0] neg_lo:[1,0,0] neg_hi:[1,0,0]
	v_pk_mul_f32 v[120:121], v[122:123], v[164:165] op_sel_hi:[1,0]
	v_pk_fma_f32 v[160:161], v[126:127], v[128:129], v[156:157] op_sel:[0,1,1] op_sel_hi:[1,1,0]
	v_pk_fma_f32 v[168:169], v[126:127], v[128:129], v[156:157] op_sel:[0,1,1] op_sel_hi:[1,1,0] neg_lo:[1,0,0] neg_hi:[1,0,0]
	v_pk_fma_f32 v[126:127], v[122:123], v[192:193], v[120:121] op_sel:[0,0,1] op_sel_hi:[1,0,0]
	v_pk_fma_f32 v[164:165], v[122:123], v[192:193], v[120:121] op_sel:[0,0,1] op_sel_hi:[1,0,0] neg_lo:[1,0,0] neg_hi:[1,0,0]
	s_cbranch_vccz .LBB0_1132
	v_mov_b32_e32 v127, v165
	v_mov_b32_e32 v125, v163
	v_mov_b32_e32 v161, v169
	v_mov_b32_e32 v167, v171
	v_pk_add_f32 v[156:157], v[166:167], 0 op_sel_hi:[1,0]
	v_pk_add_f32 v[154:155], v[160:161], 0 op_sel_hi:[1,0]
	v_pk_add_f32 v[122:123], v[124:125], 0 op_sel_hi:[1,0]
	v_pk_add_f32 v[120:121], v[126:127], 0 op_sel_hi:[1,0]
	s_branch .LBB0_1133

; __device__ __forceinline__ unsigned cvt_pk_bf16(float lo, float hi) { unsigned r; asm volatile("v_cvt_pk_bf16_f32 %0, %1, %2" : "=v"(r) : "v"(lo), "v"(hi)); return r; }
;     __device__ __forceinline__ void operator()(const f32x4 (&acc)[2][2][4][2], const Unit& u, int wr, int wc, int fr, int fq) const {
;     ...
;                     const int row = row0 + ai * HALF + m * 16, pos = row & 4095;
;                     const unsigned ro = (unsigned)(pos * 32 + i0) * 4u; const f32x4 c4 = *(const f32x4*)(cs + ro), s4 = *(const f32x4*)(sn + ro);
; #pragma unroll
;                     for (int bj = 0; bj < 2; ++bj) {
;                         const f32x4 v0 = acc[ai][bj][m][0], v1 = acc[ai][bj][m][1];
;                         float o[8];
;                         o[0] = v0[0] * c4[0] - v0[1] * s4[0]; o[1] = v0[1] * c4[0] + v0[0] * s4[0];
;                         o[2] = v0[2] * c4[1] - v0[3] * s4[1]; o[3] = v0[3] * c4[1] + v0[2] * s4[1];
;                         o[4] = v1[0] * c4[2] - v1[1] * s4[2]; o[5] = v1[1] * c4[2] + v1[0] * s4[2];
;                         o[6] = v1[2] * c4[3] - v1[3] * s4[3]; o[7] = v1[3] * c4[3] + v1[2] * s4[3];
;                         if (!isq) {
; #pragma unroll
;                             for (int e = 0; e < 8; ++e) ks[bj][e] += o[e]; }
;                         u32x4 w; w.x = cvt_pk_bf16(o[0] * sc, o[1] * sc); w.y = cvt_pk_bf16(o[2] * sc, o[3] * sc); w.z = cvt_pk_bf16(o[4] * sc, o[5] * sc); w.w = cvt_pk_bf16(o[6] * sc, o[7] * sc);
;                         *(u32x4*)(base + (unsigned)(row * 512 + bj * HALF) * 2u) = w;
.LBB0_1136:
	v_mul_f32_e32 v112, v167, v117
	v_mul_f32_e32 v114, v167, v162
	v_cvt_pk_bf16_f32 v168, v112, v114
	v_mul_f32_e32 v112, v167, v165
	v_mul_f32_e32 v114, v167, v132
	v_cvt_pk_bf16_f32 v169, v112, v114
	v_mul_f32_e32 v112, v167, v113
	v_mul_f32_e32 v113, v167, v118
	v_cvt_pk_bf16_f32 v170, v112, v113
	v_mul_f32_e32 v112, v167, v115
	v_add_u32_e32 v164, 16, v191
	v_mul_f32_e32 v113, v167, v134
	v_cvt_pk_bf16_f32 v171, v112, v113
	v_lshlrev_b32_e32 v112, 7, v164
	v_and_or_b32 v144, v112, s78, v182
	v_lshl_add_u64 v[112:113], s[54:55], 0, v[144:145]
	v_lshl_add_u64 v[116:117], s[52:53], 0, v[144:145]
	s_and_b64 vcc, exec, s[8:9]
	global_store_dwordx4 v[160:161], v[168:171], off offset:256
	s_waitcnt vmcnt(12) lgkmcnt(0)
	v_mov_b32_e32 v112, v208
	v_mov_b32_e32 v113, v209
	v_mov_b32_e32 v114, v210
	v_mov_b32_e32 v115, v211
	v_mov_b32_e32 v116, v212
	v_mov_b32_e32 v117, v213
	v_mov_b32_e32 v118, v214
	v_mov_b32_e32 v119, v215
	v_add_u32_e32 v250, 0xb0, v191
	v_lshlrev_b32_e32 v250, 7, v250
	v_and_or_b32 v250, v250, s78, v182
	global_load_dwordx4 v[208:211], v250, s[54:55]
	global_load_dwordx4 v[212:215], v250, s[52:53]
	v_pk_mul_f32 v[132:133], v[108:109], v[112:113] op_sel_hi:[1,0]
	v_pk_mul_f32 v[160:161], v[110:111], v[112:113] op_sel:[0,1]
	v_pk_mul_f32 v[168:169], v[104:105], v[114:115] op_sel_hi:[1,0]
	v_mov_b32_e32 v144, v115
	v_mov_b32_e32 v166, v119
	v_pk_fma_f32 v[134:135], v[108:109], v[116:117], v[132:133] op_sel:[0,0,1] op_sel_hi:[1,0,0]
	v_pk_fma_f32 v[162:163], v[108:109], v[116:117], v[132:133] op_sel:[0,0,1] op_sel_hi:[1,0,0] neg_lo:[1,0,0] neg_hi:[1,0,0]
	v_pk_fma_f32 v[132:133], v[110:111], v[116:117], v[160:161] op_sel:[0,1,1] op_sel_hi:[1,1,0]
	v_pk_fma_f32 v[160:161], v[110:111], v[116:117], v[160:161] op_sel:[0,1,1] op_sel_hi:[1,1,0] neg_lo:[1,0,0] neg_hi:[1,0,0]
	v_pk_fma_f32 v[108:109], v[104:105], v[118:119], v[168:169] op_sel:[0,0,1] op_sel_hi:[1,0,0]
	v_pk_fma_f32 v[110:111], v[104:105], v[118:119], v[168:169] op_sel:[0,0,1] op_sel_hi:[1,0,0] neg_lo:[1,0,0] neg_hi:[1,0,0]
	v_pk_mul_f32 v[168:169], v[106:107], v[144:145] op_sel_hi:[1,0]
	s_nop 0
	v_pk_fma_f32 v[104:105], v[106:107], v[166:167], v[168:169] op_sel:[0,0,1] op_sel_hi:[1,0,0]
	v_pk_fma_f32 v[106:107], v[106:107], v[166:167], v[168:169] op_sel:[0,0,1] op_sel_hi:[1,0,0] neg_lo:[1,0,0] neg_hi:[1,0,0]
	s_cbranch_vccnz .LBB0_1138
	v_mov_b32_e32 v105, v107
	v_mov_b32_e32 v109, v111
	v_mov_b32_e32 v133, v161
	v_mov_b32_e32 v135, v163
	v_pk_add_f32 v[156:157], v[156:157], v[134:135]
	v_pk_add_f32 v[154:155], v[154:155], v[132:133]
	v_pk_add_f32 v[122:123], v[122:123], v[108:109]
	v_pk_add_f32 v[120:121], v[120:121], v[104:105]

; __device__ __forceinline__ unsigned cvt_pk_bf16(float lo, float hi) { unsigned r; asm volatile("v_cvt_pk_bf16_f32 %0, %1, %2" : "=v"(r) : "v"(lo), "v"(hi)); return r; }
;     __device__ __forceinline__ void operator()(const f32x4 (&acc)[2][2][4][2], const Unit& u, int wr, int wc, int fr, int fq) const {
;     ...
;                     const int row = row0 + ai * HALF + m * 16, pos = row & 4095;
;                     const unsigned ro = (unsigned)(pos * 32 + i0) * 4u; const f32x4 c4 = *(const f32x4*)(cs + ro), s4 = *(const f32x4*)(sn + ro);
; #pragma unroll
;                     for (int bj = 0; bj < 2; ++bj) {
;                         const f32x4 v0 = acc[ai][bj][m][0], v1 = acc[ai][bj][m][1];
;                         float o[8];
;                         o[0] = v0[0] * c4[0] - v0[1] * s4[0]; o[1] = v0[1] * c4[0] + v0[0] * s4[0];
;                         o[2] = v0[2] * c4[1] - v0[3] * s4[1]; o[3] = v0[3] * c4[1] + v0[2] * s4[1];
;                         o[4] = v1[0] * c4[2] - v1[1] * s4[2]; o[5] = v1[1] * c4[2] + v1[0] * s4[2];
;                         o[6] = v1[2] * c4[3] - v1[3] * s4[3]; o[7] = v1[3] * c4[3] + v1[2] * s4[3];
;                         if (!isq) {
; #pragma unroll
;                             for (int e = 0; e < 8; ++e) ks[bj][e] += o[e]; }
;                         u32x4 w; w.x = cvt_pk_bf16(o[0] * sc, o[1] * sc); w.y = cvt_pk_bf16(o[2] * sc, o[3] * sc); w.z = cvt_pk_bf16(o[4] * sc, o[5] * sc); w.w = cvt_pk_bf16(o[6] * sc, o[7] * sc);
;                         *(u32x4*)(base + (unsigned)(row * 512 + bj * HALF) * 2u) = w;
.LBB0_1140:
	v_mul_f32_e32 v96, v167, v101
	v_mul_f32_e32 v98, v167, v106
	v_cvt_pk_bf16_f32 v106, v96, v98
	v_mul_f32_e32 v96, v167, v111
	v_mul_f32_e32 v98, v167, v108
	v_cvt_pk_bf16_f32 v107, v96, v98
	v_mul_f32_e32 v96, v167, v97
	v_mul_f32_e32 v97, v167, v102
	v_cvt_pk_bf16_f32 v108, v96, v97
	v_mul_f32_e32 v96, v167, v99
	v_mul_f32_e32 v97, v167, v112
	v_add_u32_e32 v112, 32, v191
	v_cvt_pk_bf16_f32 v109, v96, v97
	v_lshlrev_b32_e32 v96, 7, v112
	v_and_or_b32 v144, v96, s78, v182
	v_lshl_add_u64 v[96:97], s[54:55], 0, v[144:145]
	v_lshl_add_u64 v[100:101], s[52:53], 0, v[144:145]
	s_and_b64 vcc, exec, s[8:9]
	global_store_dwordx4 v[104:105], v[106:109], off offset:256
	s_waitcnt vmcnt(14) lgkmcnt(0)
	v_mov_b32_e32 v96, v216
	v_mov_b32_e32 v97, v217
	v_mov_b32_e32 v98, v218
	v_mov_b32_e32 v99, v219
	v_mov_b32_e32 v100, v220
	v_mov_b32_e32 v101, v221
	v_mov_b32_e32 v102, v222
	v_mov_b32_e32 v103, v223
	v_pk_mul_f32 v[104:105], v[92:93], v[96:97] op_sel_hi:[1,0]
	v_pk_mul_f32 v[108:109], v[94:95], v[96:97] op_sel:[0,1]
	v_pk_mul_f32 v[114:115], v[88:89], v[98:99] op_sel_hi:[1,0]
	v_mov_b32_e32 v116, v99
	v_mov_b32_e32 v118, v103
	v_pk_fma_f32 v[106:107], v[92:93], v[100:101], v[104:105] op_sel:[0,0,1] op_sel_hi:[1,0,0]
	v_pk_fma_f32 v[110:111], v[92:93], v[100:101], v[104:105] op_sel:[0,0,1] op_sel_hi:[1,0,0] neg_lo:[1,0,0] neg_hi:[1,0,0]
	v_pk_fma_f32 v[104:105], v[94:95], v[100:101], v[108:109] op_sel:[0,1,1] op_sel_hi:[1,1,0]
	v_pk_fma_f32 v[108:109], v[94:95], v[100:101], v[108:109] op_sel:[0,1,1] op_sel_hi:[1,1,0] neg_lo:[1,0,0] neg_hi:[1,0,0]
	v_pk_fma_f32 v[92:93], v[88:89], v[102:103], v[114:115] op_sel:[0,0,1] op_sel_hi:[1,0,0]
	v_pk_fma_f32 v[94:95], v[88:89], v[102:103], v[114:115] op_sel:[0,0,1] op_sel_hi:[1,0,0] neg_lo:[1,0,0] neg_hi:[1,0,0]
	v_pk_mul_f32 v[114:115], v[90:91], v[116:117] op_sel_hi:[1,0]
	s_nop 0
	v_pk_fma_f32 v[88:89], v[90:91], v[118:119], v[114:115] op_sel:[0,0,1] op_sel_hi:[1,0,0]
	v_pk_fma_f32 v[90:91], v[90:91], v[118:119], v[114:115] op_sel:[0,0,1] op_sel_hi:[1,0,0] neg_lo:[1,0,0] neg_hi:[1,0,0]
	s_cbranch_vccnz .LBB0_1142
	v_mov_b32_e32 v89, v91
	v_mov_b32_e32 v93, v95
	v_mov_b32_e32 v105, v109
	v_mov_b32_e32 v107, v111
	v_pk_add_f32 v[156:157], v[156:157], v[106:107]
	v_pk_add_f32 v[154:155], v[154:155], v[104:105]
	v_pk_add_f32 v[122:123], v[122:123], v[92:93]
	v_pk_add_f32 v[120:121], v[120:121], v[88:89]

; __device__ __forceinline__ unsigned cvt_pk_bf16(float lo, float hi) { unsigned r; asm volatile("v_cvt_pk_bf16_f32 %0, %1, %2" : "=v"(r) : "v"(lo), "v"(hi)); return r; }
;     __device__ __forceinline__ void operator()(const f32x4 (&acc)[2][2][4][2], const Unit& u, int wr, int wc, int fr, int fq) const {
;     ...
;                     const int row = row0 + ai * HALF + m * 16, pos = row & 4095;
;                     const unsigned ro = (unsigned)(pos * 32 + i0) * 4u; const f32x4 c4 = *(const f32x4*)(cs + ro), s4 = *(const f32x4*)(sn + ro);
; #pragma unroll
;                     for (int bj = 0; bj < 2; ++bj) {
;                         const f32x4 v0 = acc[ai][bj][m][0], v1 = acc[ai][bj][m][1];
;                         float o[8];
;                         o[0] = v0[0] * c4[0] - v0[1] * s4[0]; o[1] = v0[1] * c4[0] + v0[0] * s4[0];
;                         o[2] = v0[2] * c4[1] - v0[3] * s4[1]; o[3] = v0[3] * c4[1] + v0[2] * s4[1];
;                         o[4] = v1[0] * c4[2] - v1[1] * s4[2]; o[5] = v1[1] * c4[2] + v1[0] * s4[2];
;                         o[6] = v1[2] * c4[3] - v1[3] * s4[3]; o[7] = v1[3] * c4[3] + v1[2] * s4[3];
;                         if (!isq) {
; #pragma unroll
;                             for (int e = 0; e < 8; ++e) ks[bj][e] += o[e]; }
;                         u32x4 w; w.x = cvt_pk_bf16(o[0] * sc, o[1] * sc); w.y = cvt_pk_bf16(o[2] * sc, o[3] * sc); w.z = cvt_pk_bf16(o[4] * sc, o[5] * sc); w.w = cvt_pk_bf16(o[6] * sc, o[7] * sc);
;                         *(u32x4*)(base + (unsigned)(row * 512 + bj * HALF) * 2u) = w;
.LBB0_1144:
	v_mul_f32_e32 v80, v167, v85
	v_mul_f32_e32 v82, v167, v90
	v_cvt_pk_bf16_f32 v90, v80, v82
	v_mul_f32_e32 v80, v167, v95
	v_mul_f32_e32 v82, v167, v92
	v_cvt_pk_bf16_f32 v91, v80, v82
	v_mul_f32_e32 v80, v167, v81
	v_mul_f32_e32 v81, v167, v86
	v_cvt_pk_bf16_f32 v92, v80, v81
	v_mul_f32_e32 v80, v167, v83
	v_mul_f32_e32 v81, v167, v96
	v_add_u32_e32 v96, 48, v191
	v_cvt_pk_bf16_f32 v93, v80, v81
	v_lshlrev_b32_e32 v80, 7, v96
	v_and_or_b32 v144, v80, s78, v182
	v_lshl_add_u64 v[80:81], s[54:55], 0, v[144:145]
	v_lshl_add_u64 v[84:85], s[52:53], 0, v[144:145]
	s_and_b64 vcc, exec, s[8:9]
	global_store_dwordx4 v[88:89], v[90:93], off offset:256
	s_waitcnt vmcnt(14) lgkmcnt(0)
	v_mov_b32_e32 v80, v224
	v_mov_b32_e32 v81, v225
	v_mov_b32_e32 v82, v226
	v_mov_b32_e32 v83, v227
	v_mov_b32_e32 v84, v228
	v_mov_b32_e32 v85, v229
	v_mov_b32_e32 v86, v230
	v_mov_b32_e32 v87, v231
	v_pk_mul_f32 v[88:89], v[76:77], v[80:81] op_sel_hi:[1,0]
	v_pk_mul_f32 v[92:93], v[78:79], v[80:81] op_sel:[0,1]
	v_pk_mul_f32 v[98:99], v[72:73], v[82:83] op_sel_hi:[1,0]
	v_mov_b32_e32 v100, v83
	v_mov_b32_e32 v102, v87
	v_pk_fma_f32 v[90:91], v[76:77], v[84:85], v[88:89] op_sel:[0,0,1] op_sel_hi:[1,0,0]
	v_pk_fma_f32 v[94:95], v[76:77], v[84:85], v[88:89] op_sel:[0,0,1] op_sel_hi:[1,0,0] neg_lo:[1,0,0] neg_hi:[1,0,0]
	v_pk_fma_f32 v[88:89], v[78:79], v[84:85], v[92:93] op_sel:[0,1,1] op_sel_hi:[1,1,0]
	v_pk_fma_f32 v[92:93], v[78:79], v[84:85], v[92:93] op_sel:[0,1,1] op_sel_hi:[1,1,0] neg_lo:[1,0,0] neg_hi:[1,0,0]
	v_pk_fma_f32 v[76:77], v[72:73], v[86:87], v[98:99] op_sel:[0,0,1] op_sel_hi:[1,0,0]
	v_pk_fma_f32 v[78:79], v[72:73], v[86:87], v[98:99] op_sel:[0,0,1] op_sel_hi:[1,0,0] neg_lo:[1,0,0] neg_hi:[1,0,0]
	v_pk_mul_f32 v[98:99], v[74:75], v[100:101] op_sel_hi:[1,0]
	s_nop 0
	v_pk_fma_f32 v[72:73], v[74:75], v[102:103], v[98:99] op_sel:[0,0,1] op_sel_hi:[1,0,0]
	v_pk_fma_f32 v[74:75], v[74:75], v[102:103], v[98:99] op_sel:[0,0,1] op_sel_hi:[1,0,0] neg_lo:[1,0,0] neg_hi:[1,0,0]
	s_cbranch_vccnz .LBB0_1146
	v_mov_b32_e32 v73, v75
	v_mov_b32_e32 v77, v79
	v_mov_b32_e32 v89, v93
	v_mov_b32_e32 v91, v95
	v_pk_add_f32 v[156:157], v[156:157], v[90:91]
	v_pk_add_f32 v[154:155], v[154:155], v[88:89]
	v_pk_add_f32 v[122:123], v[122:123], v[76:77]
	v_pk_add_f32 v[120:121], v[120:121], v[72:73]

; __device__ __forceinline__ unsigned cvt_pk_bf16(float lo, float hi) { unsigned r; asm volatile("v_cvt_pk_bf16_f32 %0, %1, %2" : "=v"(r) : "v"(lo), "v"(hi)); return r; }
;     __device__ __forceinline__ void operator()(const f32x4 (&acc)[2][2][4][2], const Unit& u, int wr, int wc, int fr, int fq) const {
;     ...
;                     const int row = row0 + ai * HALF + m * 16, pos = row & 4095;
;                     const unsigned ro = (unsigned)(pos * 32 + i0) * 4u; const f32x4 c4 = *(const f32x4*)(cs + ro), s4 = *(const f32x4*)(sn + ro);
; #pragma unroll
;                     for (int bj = 0; bj < 2; ++bj) {
;                         const f32x4 v0 = acc[ai][bj][m][0], v1 = acc[ai][bj][m][1];
;                         float o[8];
;                         o[0] = v0[0] * c4[0] - v0[1] * s4[0]; o[1] = v0[1] * c4[0] + v0[0] * s4[0];
;                         o[2] = v0[2] * c4[1] - v0[3] * s4[1]; o[3] = v0[3] * c4[1] + v0[2] * s4[1];
;                         o[4] = v1[0] * c4[2] - v1[1] * s4[2]; o[5] = v1[1] * c4[2] + v1[0] * s4[2];
;                         o[6] = v1[2] * c4[3] - v1[3] * s4[3]; o[7] = v1[3] * c4[3] + v1[2] * s4[3];
;                         if (!isq) {
; #pragma unroll
;                             for (int e = 0; e < 8; ++e) ks[bj][e] += o[e]; }
;                         u32x4 w; w.x = cvt_pk_bf16(o[0] * sc, o[1] * sc); w.y = cvt_pk_bf16(o[2] * sc, o[3] * sc); w.z = cvt_pk_bf16(o[4] * sc, o[5] * sc); w.w = cvt_pk_bf16(o[6] * sc, o[7] * sc);
;                         *(u32x4*)(base + (unsigned)(row * 512 + bj * HALF) * 2u) = w;
.LBB0_1148:
	v_mul_f32_e32 v64, v167, v69
	v_mul_f32_e32 v66, v167, v74
	v_cvt_pk_bf16_f32 v74, v64, v66
	v_mul_f32_e32 v64, v167, v79
	v_mul_f32_e32 v66, v167, v76
	v_cvt_pk_bf16_f32 v75, v64, v66
	v_mul_f32_e32 v64, v167, v65
	v_mul_f32_e32 v65, v167, v70
	v_cvt_pk_bf16_f32 v76, v64, v65
	v_mul_f32_e32 v64, v167, v67
	v_mul_f32_e32 v65, v167, v80
	v_add_u32_e32 v80, 0x80, v191
	v_cvt_pk_bf16_f32 v77, v64, v65
	v_lshlrev_b32_e32 v64, 7, v80
	v_and_or_b32 v144, v64, s78, v182
	v_lshl_add_u64 v[64:65], s[54:55], 0, v[144:145]
	v_lshl_add_u64 v[68:69], s[52:53], 0, v[144:145]
	s_and_b64 vcc, exec, s[8:9]
	global_store_dwordx4 v[72:73], v[74:77], off offset:256
	s_waitcnt vmcnt(14) lgkmcnt(0)
	v_mov_b32_e32 v64, v232
	v_mov_b32_e32 v65, v233
	v_mov_b32_e32 v66, v234
	v_mov_b32_e32 v67, v235
	v_mov_b32_e32 v68, v236
	v_mov_b32_e32 v69, v237
	v_mov_b32_e32 v70, v238
	v_mov_b32_e32 v71, v239
	v_pk_mul_f32 v[72:73], v[60:61], v[64:65] op_sel_hi:[1,0]
	v_pk_mul_f32 v[76:77], v[62:63], v[64:65] op_sel:[0,1]
	v_pk_mul_f32 v[82:83], v[56:57], v[66:67] op_sel_hi:[1,0]
	v_mov_b32_e32 v84, v67
	v_mov_b32_e32 v86, v71
	v_pk_fma_f32 v[74:75], v[60:61], v[68:69], v[72:73] op_sel:[0,0,1] op_sel_hi:[1,0,0]
	v_pk_fma_f32 v[78:79], v[60:61], v[68:69], v[72:73] op_sel:[0,0,1] op_sel_hi:[1,0,0] neg_lo:[1,0,0] neg_hi:[1,0,0]
	v_pk_fma_f32 v[72:73], v[62:63], v[68:69], v[76:77] op_sel:[0,1,1] op_sel_hi:[1,1,0]
	v_pk_fma_f32 v[76:77], v[62:63], v[68:69], v[76:77] op_sel:[0,1,1] op_sel_hi:[1,1,0] neg_lo:[1,0,0] neg_hi:[1,0,0]
	v_pk_fma_f32 v[60:61], v[56:57], v[70:71], v[82:83] op_sel:[0,0,1] op_sel_hi:[1,0,0]
	v_pk_fma_f32 v[62:63], v[56:57], v[70:71], v[82:83] op_sel:[0,0,1] op_sel_hi:[1,0,0] neg_lo:[1,0,0] neg_hi:[1,0,0]
	v_pk_mul_f32 v[82:83], v[58:59], v[84:85] op_sel_hi:[1,0]
	s_nop 0
	v_pk_fma_f32 v[56:57], v[58:59], v[86:87], v[82:83] op_sel:[0,0,1] op_sel_hi:[1,0,0]
	v_pk_fma_f32 v[58:59], v[58:59], v[86:87], v[82:83] op_sel:[0,0,1] op_sel_hi:[1,0,0] neg_lo:[1,0,0] neg_hi:[1,0,0]
	s_cbranch_vccnz .LBB0_1150
	v_mov_b32_e32 v57, v59
	v_mov_b32_e32 v61, v63
	v_mov_b32_e32 v73, v77
	v_mov_b32_e32 v75, v79
	v_pk_add_f32 v[156:157], v[156:157], v[74:75]
	v_pk_add_f32 v[154:155], v[154:155], v[72:73]
	v_pk_add_f32 v[122:123], v[122:123], v[60:61]
	v_pk_add_f32 v[120:121], v[120:121], v[56:57]

; __device__ __forceinline__ unsigned cvt_pk_bf16(float lo, float hi) { unsigned r; asm volatile("v_cvt_pk_bf16_f32 %0, %1, %2" : "=v"(r) : "v"(lo), "v"(hi)); return r; }
;     __device__ __forceinline__ void operator()(const f32x4 (&acc)[2][2][4][2], const Unit& u, int wr, int wc, int fr, int fq) const {
;     ...
;                     const int row = row0 + ai * HALF + m * 16, pos = row & 4095;
;                     const unsigned ro = (unsigned)(pos * 32 + i0) * 4u; const f32x4 c4 = *(const f32x4*)(cs + ro), s4 = *(const f32x4*)(sn + ro);
; #pragma unroll
;                     for (int bj = 0; bj < 2; ++bj) {
;                         const f32x4 v0 = acc[ai][bj][m][0], v1 = acc[ai][bj][m][1];
;                         float o[8];
;                         o[0] = v0[0] * c4[0] - v0[1] * s4[0]; o[1] = v0[1] * c4[0] + v0[0] * s4[0];
;                         o[2] = v0[2] * c4[1] - v0[3] * s4[1]; o[3] = v0[3] * c4[1] + v0[2] * s4[1];
;                         o[4] = v1[0] * c4[2] - v1[1] * s4[2]; o[5] = v1[1] * c4[2] + v1[0] * s4[2];
;                         o[6] = v1[2] * c4[3] - v1[3] * s4[3]; o[7] = v1[3] * c4[3] + v1[2] * s4[3];
;                         if (!isq) {
; #pragma unroll
;                             for (int e = 0; e < 8; ++e) ks[bj][e] += o[e]; }
;                         u32x4 w; w.x = cvt_pk_bf16(o[0] * sc, o[1] * sc); w.y = cvt_pk_bf16(o[2] * sc, o[3] * sc); w.z = cvt_pk_bf16(o[4] * sc, o[5] * sc); w.w = cvt_pk_bf16(o[6] * sc, o[7] * sc);
;                         *(u32x4*)(base + (unsigned)(row * 512 + bj * HALF) * 2u) = w;
.LBB0_1152:
	v_mul_f32_e32 v48, v167, v53
	v_mul_f32_e32 v50, v167, v58
	v_cvt_pk_bf16_f32 v58, v48, v50
	v_mul_f32_e32 v48, v167, v63
	v_mul_f32_e32 v50, v167, v60
	v_cvt_pk_bf16_f32 v59, v48, v50
	v_mul_f32_e32 v48, v167, v49
	v_mul_f32_e32 v49, v167, v54
	v_cvt_pk_bf16_f32 v60, v48, v49
	v_mul_f32_e32 v48, v167, v51
	v_mul_f32_e32 v49, v167, v64
	v_add_u32_e32 v64, 0x90, v191
	v_cvt_pk_bf16_f32 v61, v48, v49
	v_lshlrev_b32_e32 v48, 7, v64
	v_and_or_b32 v144, v48, s78, v182
	v_lshl_add_u64 v[48:49], s[54:55], 0, v[144:145]
	v_lshl_add_u64 v[52:53], s[52:53], 0, v[144:145]
	s_and_b64 vcc, exec, s[8:9]
	global_store_dwordx4 v[56:57], v[58:61], off offset:256
	s_waitcnt vmcnt(14) lgkmcnt(0)
	v_mov_b32_e32 v48, v240
	v_mov_b32_e32 v49, v241
	v_mov_b32_e32 v50, v242
	v_mov_b32_e32 v51, v243
	v_mov_b32_e32 v52, v244
	v_mov_b32_e32 v53, v245
	v_mov_b32_e32 v54, v246
	v_mov_b32_e32 v55, v247
	v_pk_mul_f32 v[56:57], v[44:45], v[48:49] op_sel_hi:[1,0]
	v_pk_mul_f32 v[60:61], v[46:47], v[48:49] op_sel:[0,1]
	v_pk_mul_f32 v[66:67], v[40:41], v[50:51] op_sel_hi:[1,0]
	v_mov_b32_e32 v68, v51
	v_mov_b32_e32 v70, v55
	v_pk_fma_f32 v[58:59], v[44:45], v[52:53], v[56:57] op_sel:[0,0,1] op_sel_hi:[1,0,0]
	v_pk_fma_f32 v[62:63], v[44:45], v[52:53], v[56:57] op_sel:[0,0,1] op_sel_hi:[1,0,0] neg_lo:[1,0,0] neg_hi:[1,0,0]
	v_pk_fma_f32 v[56:57], v[46:47], v[52:53], v[60:61] op_sel:[0,1,1] op_sel_hi:[1,1,0]
	v_pk_fma_f32 v[60:61], v[46:47], v[52:53], v[60:61] op_sel:[0,1,1] op_sel_hi:[1,1,0] neg_lo:[1,0,0] neg_hi:[1,0,0]
	v_pk_fma_f32 v[44:45], v[40:41], v[54:55], v[66:67] op_sel:[0,0,1] op_sel_hi:[1,0,0]
	v_pk_fma_f32 v[46:47], v[40:41], v[54:55], v[66:67] op_sel:[0,0,1] op_sel_hi:[1,0,0] neg_lo:[1,0,0] neg_hi:[1,0,0]
	v_pk_mul_f32 v[66:67], v[42:43], v[68:69] op_sel_hi:[1,0]
	s_nop 0
	v_pk_fma_f32 v[40:41], v[42:43], v[70:71], v[66:67] op_sel:[0,0,1] op_sel_hi:[1,0,0]
	v_pk_fma_f32 v[42:43], v[42:43], v[70:71], v[66:67] op_sel:[0,0,1] op_sel_hi:[1,0,0] neg_lo:[1,0,0] neg_hi:[1,0,0]
	s_cbranch_vccnz .LBB0_1154
	v_mov_b32_e32 v41, v43
	v_mov_b32_e32 v45, v47
	v_mov_b32_e32 v57, v61
	v_mov_b32_e32 v59, v63
	v_pk_add_f32 v[156:157], v[156:157], v[58:59]
	v_pk_add_f32 v[154:155], v[154:155], v[56:57]
	v_pk_add_f32 v[122:123], v[122:123], v[44:45]
	v_pk_add_f32 v[120:121], v[120:121], v[40:41]

; __device__ __forceinline__ unsigned cvt_pk_bf16(float lo, float hi) { unsigned r; asm volatile("v_cvt_pk_bf16_f32 %0, %1, %2" : "=v"(r) : "v"(lo), "v"(hi)); return r; }
;     __device__ __forceinline__ void operator()(const f32x4 (&acc)[2][2][4][2], const Unit& u, int wr, int wc, int fr, int fq) const {
;     ...
;                     const int row = row0 + ai * HALF + m * 16, pos = row & 4095;
;                     const unsigned ro = (unsigned)(pos * 32 + i0) * 4u; const f32x4 c4 = *(const f32x4*)(cs + ro), s4 = *(const f32x4*)(sn + ro);
; #pragma unroll
;                     for (int bj = 0; bj < 2; ++bj) {
;                         const f32x4 v0 = acc[ai][bj][m][0], v1 = acc[ai][bj][m][1];
;                         float o[8];
;                         o[0] = v0[0] * c4[0] - v0[1] * s4[0]; o[1] = v0[1] * c4[0] + v0[0] * s4[0];
;                         o[2] = v0[2] * c4[1] - v0[3] * s4[1]; o[3] = v0[3] * c4[1] + v0[2] * s4[1];
;                         o[4] = v1[0] * c4[2] - v1[1] * s4[2]; o[5] = v1[1] * c4[2] + v1[0] * s4[2];
;                         o[6] = v1[2] * c4[3] - v1[3] * s4[3]; o[7] = v1[3] * c4[3] + v1[2] * s4[3];
;                         if (!isq) {
; #pragma unroll
;                             for (int e = 0; e < 8; ++e) ks[bj][e] += o[e]; }
;                         u32x4 w; w.x = cvt_pk_bf16(o[0] * sc, o[1] * sc); w.y = cvt_pk_bf16(o[2] * sc, o[3] * sc); w.z = cvt_pk_bf16(o[4] * sc, o[5] * sc); w.w = cvt_pk_bf16(o[6] * sc, o[7] * sc);
;                         *(u32x4*)(base + (unsigned)(row * 512 + bj * HALF) * 2u) = w;
.LBB0_1156:
	v_mul_f32_e32 v32, v167, v37
	v_mul_f32_e32 v34, v167, v42
	v_cvt_pk_bf16_f32 v42, v32, v34
	v_mul_f32_e32 v32, v167, v47
	v_mul_f32_e32 v34, v167, v44
	v_cvt_pk_bf16_f32 v43, v32, v34
	v_mul_f32_e32 v32, v167, v33
	v_mul_f32_e32 v33, v167, v38
	v_cvt_pk_bf16_f32 v44, v32, v33
	v_mul_f32_e32 v32, v167, v35
	v_mul_f32_e32 v33, v167, v48
	v_add_u32_e32 v48, 0xa0, v191
	v_cvt_pk_bf16_f32 v45, v32, v33
	v_lshlrev_b32_e32 v32, 7, v48
	v_and_or_b32 v144, v32, s78, v182
	v_lshl_add_u64 v[32:33], s[54:55], 0, v[144:145]
	v_lshl_add_u64 v[36:37], s[52:53], 0, v[144:145]
	s_and_b64 vcc, exec, s[8:9]
	global_store_dwordx4 v[40:41], v[42:45], off offset:256
	s_waitcnt vmcnt(14) lgkmcnt(0)
	v_mov_b32_e32 v32, v200
	v_mov_b32_e32 v33, v201
	v_mov_b32_e32 v34, v202
	v_mov_b32_e32 v35, v203
	v_mov_b32_e32 v36, v204
	v_mov_b32_e32 v37, v205
	v_mov_b32_e32 v38, v206
	v_mov_b32_e32 v39, v207
	v_pk_mul_f32 v[40:41], v[28:29], v[32:33] op_sel_hi:[1,0]
	v_pk_mul_f32 v[44:45], v[30:31], v[32:33] op_sel:[0,1]
	v_pk_mul_f32 v[50:51], v[24:25], v[34:35] op_sel_hi:[1,0]
	v_mov_b32_e32 v52, v35
	v_mov_b32_e32 v54, v39
	v_pk_fma_f32 v[42:43], v[28:29], v[36:37], v[40:41] op_sel:[0,0,1] op_sel_hi:[1,0,0]
	v_pk_fma_f32 v[46:47], v[28:29], v[36:37], v[40:41] op_sel:[0,0,1] op_sel_hi:[1,0,0] neg_lo:[1,0,0] neg_hi:[1,0,0]
	v_pk_fma_f32 v[40:41], v[30:31], v[36:37], v[44:45] op_sel:[0,1,1] op_sel_hi:[1,1,0]
	v_pk_fma_f32 v[44:45], v[30:31], v[36:37], v[44:45] op_sel:[0,1,1] op_sel_hi:[1,1,0] neg_lo:[1,0,0] neg_hi:[1,0,0]
	v_pk_fma_f32 v[28:29], v[24:25], v[38:39], v[50:51] op_sel:[0,0,1] op_sel_hi:[1,0,0]
	v_pk_fma_f32 v[30:31], v[24:25], v[38:39], v[50:51] op_sel:[0,0,1] op_sel_hi:[1,0,0] neg_lo:[1,0,0] neg_hi:[1,0,0]
	v_pk_mul_f32 v[50:51], v[26:27], v[52:53] op_sel_hi:[1,0]
	s_nop 0
	v_pk_fma_f32 v[24:25], v[26:27], v[54:55], v[50:51] op_sel:[0,0,1] op_sel_hi:[1,0,0]
	v_pk_fma_f32 v[26:27], v[26:27], v[54:55], v[50:51] op_sel:[0,0,1] op_sel_hi:[1,0,0] neg_lo:[1,0,0] neg_hi:[1,0,0]
	s_cbranch_vccnz .LBB0_1158
	v_mov_b32_e32 v25, v27
	v_mov_b32_e32 v29, v31
	v_mov_b32_e32 v41, v45
	v_mov_b32_e32 v43, v47
	v_pk_add_f32 v[156:157], v[156:157], v[42:43]
	v_pk_add_f32 v[154:155], v[154:155], v[40:41]
	v_pk_add_f32 v[122:123], v[122:123], v[28:29]
	v_pk_add_f32 v[120:121], v[120:121], v[24:25]

; __device__ __forceinline__ unsigned cvt_pk_bf16(float lo, float hi) { unsigned r; asm volatile("v_cvt_pk_bf16_f32 %0, %1, %2" : "=v"(r) : "v"(lo), "v"(hi)); return r; }
;     __device__ __forceinline__ void operator()(const f32x4 (&acc)[2][2][4][2], const Unit& u, int wr, int wc, int fr, int fq) const {
;     ...
;                     const int row = row0 + ai * HALF + m * 16, pos = row & 4095;
;                     const unsigned ro = (unsigned)(pos * 32 + i0) * 4u; const f32x4 c4 = *(const f32x4*)(cs + ro), s4 = *(const f32x4*)(sn + ro);
; #pragma unroll
;                     for (int bj = 0; bj < 2; ++bj) {
;                         const f32x4 v0 = acc[ai][bj][m][0], v1 = acc[ai][bj][m][1];
;                         float o[8];
;                         o[0] = v0[0] * c4[0] - v0[1] * s4[0]; o[1] = v0[1] * c4[0] + v0[0] * s4[0];
;                         o[2] = v0[2] * c4[1] - v0[3] * s4[1]; o[3] = v0[3] * c4[1] + v0[2] * s4[1];
;                         o[4] = v1[0] * c4[2] - v1[1] * s4[2]; o[5] = v1[1] * c4[2] + v1[0] * s4[2];
;                         o[6] = v1[2] * c4[3] - v1[3] * s4[3]; o[7] = v1[3] * c4[3] + v1[2] * s4[3];
;                         if (!isq) {
; #pragma unroll
;                             for (int e = 0; e < 8; ++e) ks[bj][e] += o[e]; }
;                         u32x4 w; w.x = cvt_pk_bf16(o[0] * sc, o[1] * sc); w.y = cvt_pk_bf16(o[2] * sc, o[3] * sc); w.z = cvt_pk_bf16(o[4] * sc, o[5] * sc); w.w = cvt_pk_bf16(o[6] * sc, o[7] * sc);
;                         *(u32x4*)(base + (unsigned)(row * 512 + bj * HALF) * 2u) = w;
.LBB0_1160:
	v_mul_f32_e32 v16, v167, v21
	v_mul_f32_e32 v18, v167, v26
	v_cvt_pk_bf16_f32 v26, v16, v18
	v_mul_f32_e32 v16, v167, v31
	v_mul_f32_e32 v18, v167, v28
	v_cvt_pk_bf16_f32 v27, v16, v18
	v_mul_f32_e32 v16, v167, v17
	v_mul_f32_e32 v17, v167, v22
	v_cvt_pk_bf16_f32 v28, v16, v17
	v_mul_f32_e32 v16, v167, v19
	v_mul_f32_e32 v17, v167, v32
	v_add_u32_e32 v32, 0xb0, v191
	v_cvt_pk_bf16_f32 v29, v16, v17
	v_lshlrev_b32_e32 v16, 7, v32
	v_and_or_b32 v144, v16, s78, v182
	v_lshl_add_u64 v[16:17], s[54:55], 0, v[144:145]
	v_lshl_add_u64 v[20:21], s[52:53], 0, v[144:145]
	s_and_b64 vcc, exec, s[8:9]
	global_store_dwordx4 v[24:25], v[26:29], off offset:256
	s_waitcnt vmcnt(12) lgkmcnt(0)
	v_mov_b32_e32 v16, v208
	v_mov_b32_e32 v17, v209
	v_mov_b32_e32 v18, v210
	v_mov_b32_e32 v19, v211
	v_mov_b32_e32 v20, v212
	v_mov_b32_e32 v21, v213
	v_mov_b32_e32 v22, v214
	v_mov_b32_e32 v23, v215
	v_pk_mul_f32 v[24:25], v[12:13], v[16:17] op_sel_hi:[1,0]
	v_pk_mul_f32 v[28:29], v[14:15], v[16:17] op_sel:[0,1]
	v_pk_mul_f32 v[34:35], v[8:9], v[18:19] op_sel_hi:[1,0]
	v_mov_b32_e32 v36, v19
	v_mov_b32_e32 v38, v23
	v_pk_fma_f32 v[26:27], v[12:13], v[20:21], v[24:25] op_sel:[0,0,1] op_sel_hi:[1,0,0]
	v_pk_fma_f32 v[30:31], v[12:13], v[20:21], v[24:25] op_sel:[0,0,1] op_sel_hi:[1,0,0] neg_lo:[1,0,0] neg_hi:[1,0,0]
	v_pk_fma_f32 v[24:25], v[14:15], v[20:21], v[28:29] op_sel:[0,1,1] op_sel_hi:[1,1,0]
	v_pk_fma_f32 v[28:29], v[14:15], v[20:21], v[28:29] op_sel:[0,1,1] op_sel_hi:[1,1,0] neg_lo:[1,0,0] neg_hi:[1,0,0]
	v_pk_fma_f32 v[12:13], v[8:9], v[22:23], v[34:35] op_sel:[0,0,1] op_sel_hi:[1,0,0]
	v_pk_fma_f32 v[14:15], v[8:9], v[22:23], v[34:35] op_sel:[0,0,1] op_sel_hi:[1,0,0] neg_lo:[1,0,0] neg_hi:[1,0,0]
	v_pk_mul_f32 v[34:35], v[10:11], v[36:37] op_sel_hi:[1,0]
	s_nop 0
	v_pk_fma_f32 v[8:9], v[10:11], v[38:39], v[34:35] op_sel:[0,0,1] op_sel_hi:[1,0,0]
	v_pk_fma_f32 v[10:11], v[10:11], v[38:39], v[34:35] op_sel:[0,0,1] op_sel_hi:[1,0,0] neg_lo:[1,0,0] neg_hi:[1,0,0]
	s_cbranch_vccnz .LBB0_1162
	v_mov_b32_e32 v9, v11
	v_mov_b32_e32 v13, v15
	v_mov_b32_e32 v25, v29
	v_mov_b32_e32 v27, v31
	v_pk_add_f32 v[156:157], v[156:157], v[26:27]
	v_pk_add_f32 v[154:155], v[154:155], v[24:25]
	v_pk_add_f32 v[122:123], v[122:123], v[12:13]
	v_pk_add_f32 v[120:121], v[120:121], v[8:9]

;     __device__ __forceinline__ void operator()(const f32x4 (&acc)[2][2][4][2], const Unit& u, int wr, int wc, int fr, int fq) const {
;     ...
;                         *(u32x4*)(base + (unsigned)(row * 512 + bj * HALF) * 2u) = w;
;                     }
;                 }
;             if (!isq) {
; #pragma unroll
;                 for (int bj = 0; bj < 2; ++bj)
; #pragma unroll
;                     for (int e = 0; e < 8; ++e) { float s = ks[bj][e]; s += __shfl_xor(s, 1); s += __shfl_xor(s, 2); s += __shfl_xor(s, 4); s += __shfl_xor(s, 8); ks[bj][e] = s; }
;                 if (fr == 0 && do_km) {
;                     const int b = u.pm >> 4, nb = u.pm & 15;
; #pragma unroll
;                     for (int bj = 0; bj < 2; ++bj) { const int h = (pn & 1) * 4 + 2 * bj + (wc >> 1); float* kp = (float*)(wb + OFF_KMEAN + (unsigned)(layer * 32768 + ((b * 8 + h) * 16 + nb) * 64 + 32 * (wc & 1) + 8 * fq) * 4u);
; #pragma unroll
;                         for (int e = 0; e < 8; ++e) unsafeAtomicAdd(kp + e, ks[bj][e] * (1.0f / 256.0f)); }
.LBB0_1164:
	v_mul_f32_e32 v0, v167, v5
	v_mul_f32_e32 v2, v167, v10
	v_cvt_pk_bf16_f32 v4, v0, v2
	v_mul_f32_e32 v0, v167, v15
	v_mul_f32_e32 v2, v167, v12
	v_cvt_pk_bf16_f32 v5, v0, v2
	v_mul_f32_e32 v0, v167, v1
	v_mul_f32_e32 v1, v167, v6
	s_and_b64 vcc, exec, s[50:51]
	v_cvt_pk_bf16_f32 v6, v0, v1
	v_mul_f32_e32 v0, v167, v3
	v_mul_f32_e32 v1, v167, v16
	v_cvt_pk_bf16_f32 v7, v0, v1
	global_store_dwordx4 v[8:9], v[4:7], off offset:256
	s_cbranch_vccz .LBB0_1168
	ds_bpermute_b32 v1, v173, v156
	ds_bpermute_b32 v2, v173, v155
	ds_bpermute_b32 v5, v173, v154
	ds_bpermute_b32 v8, v173, v123
	ds_bpermute_b32 v11, v173, v122
	s_waitcnt lgkmcnt(0)
	v_add_f32_e32 v1, v156, v1
	ds_bpermute_b32 v4, v174, v1
	v_add_f32_e32 v6, v155, v2
	v_add_f32_e32 v8, v123, v8
	ds_bpermute_b32 v10, v174, v8
	ds_bpermute_b32 v18, v173, v130
	s_waitcnt lgkmcnt(0)
	v_add_f32_e32 v1, v1, v4
	v_add_f32_e32 v4, v154, v5
	ds_bpermute_b32 v5, v174, v6
	ds_bpermute_b32 v7, v174, v4
	v_add_f32_e32 v8, v8, v10
	v_add_f32_e32 v11, v122, v11
	ds_bpermute_b32 v10, v175, v8
	s_waitcnt lgkmcnt(0)
	v_add_f32_e32 v5, v6, v5
	v_add_f32_e32 v7, v4, v7
	ds_bpermute_b32 v6, v175, v5
	ds_bpermute_b32 v9, v175, v7
	ds_bpermute_b32 v12, v174, v11
	v_add_f32_e32 v18, v130, v18
	ds_bpermute_b32 v20, v174, v18
	s_waitcnt lgkmcnt(0)
	v_add_f32_e32 v4, v5, v6
	v_add_f32_e32 v6, v7, v9
	ds_bpermute_b32 v9, v173, v121
	ds_bpermute_b32 v21, v173, v129
	v_add_f32_e32 v8, v8, v10
	v_add_f32_e32 v10, v11, v12
	ds_bpermute_b32 v15, v173, v131
	s_waitcnt lgkmcnt(0)
	v_add_f32_e32 v13, v121, v9
	ds_bpermute_b32 v14, v174, v13
	v_add_f32_e32 v18, v18, v20
	v_add_f32_e32 v20, v129, v21
	v_add_f32_e32 v15, v131, v15
	ds_bpermute_b32 v21, v174, v20
	s_waitcnt lgkmcnt(0)
	v_add_f32_e32 v12, v13, v14
	ds_bpermute_b32 v14, v173, v120
	ds_bpermute_b32 v22, v173, v128
	ds_bpermute_b32 v17, v174, v15
	v_add_f32_e32 v20, v20, v21
	ds_bpermute_b32 v0, v173, v157
	s_waitcnt lgkmcnt(0)
	v_add_f32_e32 v14, v120, v14
	ds_bpermute_b32 v16, v174, v14
	v_add_f32_e32 v21, v128, v22
	v_add_f32_e32 v17, v15, v17
	ds_bpermute_b32 v22, v174, v21
	ds_bpermute_b32 v19, v175, v17
	s_waitcnt lgkmcnt(0)
	v_add_f32_e32 v14, v14, v16
	ds_bpermute_b32 v16, v175, v14
	ds_bpermute_b32 v27, v173, v125
	v_add_f32_e32 v22, v21, v22
	ds_bpermute_b32 v26, v175, v22
	ds_bpermute_b32 v28, v173, v124
	s_waitcnt lgkmcnt(0)
	v_add_f32_e32 v14, v14, v16
	v_add_f32_e32 v16, v17, v19
	ds_bpermute_b32 v19, v175, v18
	v_add_f32_e32 v22, v22, v26
	ds_bpermute_b32 v26, v173, v126
	v_add_f32_e32 v0, v157, v0
	v_add_f32_e32 v27, v125, v27
	s_waitcnt lgkmcnt(0)
	v_add_f32_e32 v18, v18, v19
	ds_bpermute_b32 v19, v173, v127
	v_add_f32_e32 v26, v126, v26
	v_add_f32_e32 v28, v124, v28
	ds_bpermute_b32 v3, v174, v0
	ds_bpermute_b32 v29, v174, v26
	s_waitcnt lgkmcnt(0)
	v_add_f32_e32 v24, v127, v19
	ds_bpermute_b32 v25, v174, v24
	ds_bpermute_b32 v30, v174, v27
	ds_bpermute_b32 v31, v174, v28
	v_add_f32_e32 v0, v0, v3
	v_add_f32_e32 v26, v26, v29
	s_waitcnt lgkmcnt(0)
	v_add_f32_e32 v24, v24, v25
	v_add_f32_e32 v30, v27, v30
	v_add_f32_e32 v31, v28, v31
	ds_bpermute_b32 v2, v175, v0
	ds_bpermute_b32 v3, v175, v1
	ds_bpermute_b32 v11, v175, v10
	ds_bpermute_b32 v13, v175, v12
	ds_bpermute_b32 v23, v175, v20
	ds_bpermute_b32 v25, v175, v24
	ds_bpermute_b32 v29, v175, v26
	ds_bpermute_b32 v32, v175, v30
	ds_bpermute_b32 v33, v175, v31
	s_waitcnt lgkmcnt(0)
	v_add_f32_e32 v0, v0, v2
	v_add_f32_e32 v2, v1, v3
	v_add_f32_e32 v10, v10, v11
	v_add_f32_e32 v12, v12, v13
	v_add_f32_e32 v20, v20, v23
	v_add_f32_e32 v24, v24, v25
	v_add_f32_e32 v26, v26, v29
	v_add_f32_e32 v28, v30, v32
	v_add_f32_e32 v30, v31, v33
	ds_bpermute_b32 v1, v176, v0
	ds_bpermute_b32 v3, v176, v2
	ds_bpermute_b32 v5, v176, v4
	ds_bpermute_b32 v7, v176, v6
	ds_bpermute_b32 v9, v176, v8
	ds_bpermute_b32 v11, v176, v10
	ds_bpermute_b32 v13, v176, v12
	ds_bpermute_b32 v15, v176, v14
	ds_bpermute_b32 v17, v176, v16
	ds_bpermute_b32 v19, v176, v18
	ds_bpermute_b32 v21, v176, v20
	ds_bpermute_b32 v23, v176, v22
	ds_bpermute_b32 v25, v176, v24
	ds_bpermute_b32 v27, v176, v26
	ds_bpermute_b32 v29, v176, v28
	ds_bpermute_b32 v31, v176, v30
	s_and_saveexec_b64 s[8:9], s[4:5]
	s_cbranch_execz .LBB0_1167
	s_lshl_b32 s27, s27, 2
	s_or_b32 s27, s27, s73
	s_add_u32 s34, s46, 0x80000
	s_addc_u32 s35, s47, 0
	s_lshr_b32 s29, s14, 1
	s_and_b32 s29, s29, 0x3ffff8
	s_lshl_b32 s14, s14, 6
	s_or_b32 s27, s27, s29
	s_and_b32 s14, s14, 0x3c0
	s_or_b32 s14, s14, s74
	s_lshl_b32 s27, s27, 10
	s_or_b32 s29, s14, s27
	s_waitcnt lgkmcnt(0)
	v_add_f32_e32 v2, v2, v3
	v_add_f32_e32 v3, v0, v1
	v_or_b32_e32 v0, s29, v179
	v_lshl_add_u32 v144, v0, 2, v189
	v_lshl_add_u64 v[0:1], s[34:35], 0, v[144:145]
	v_mul_f32_e32 v3, 0x3b800000, v3
	v_add_f32_e32 v4, v4, v5
	flat_atomic_add_f32 v[0:1], v3
	v_mul_f32_e32 v2, 0x3b800000, v2
	v_add_f32_e32 v6, v6, v7
	flat_atomic_add_f32 v[0:1], v2 offset:4
	v_mul_f32_e32 v2, 0x3b800000, v4
	v_add_f32_e32 v8, v8, v9
	flat_atomic_add_f32 v[0:1], v2 offset:8
	v_mul_f32_e32 v2, 0x3b800000, v6
	v_add_f32_e32 v10, v10, v11
	flat_atomic_add_f32 v[0:1], v2 offset:12
	v_mul_f32_e32 v2, 0x3b800000, v8
	v_add_f32_e32 v12, v12, v13
	flat_atomic_add_f32 v[0:1], v2 offset:16
	v_mul_f32_e32 v2, 0x3b800000, v10
	v_add_f32_e32 v14, v14, v15
	flat_atomic_add_f32 v[0:1], v2 offset:20
	v_mul_f32_e32 v2, 0x3b800000, v12
	flat_atomic_add_f32 v[0:1], v2 offset:24
	v_mul_f32_e32 v2, 0x3b800000, v14
	flat_atomic_add_f32 v[0:1], v2 offset:28
	v_or_b32_e32 v0, s14, v179
	v_or_b32_e32 v0, s27, v0
	v_add_f32_e32 v16, v16, v17
	v_lshl_add_u32 v144, v0, 2, v190
	v_add_f32_e32 v18, v18, v19
	v_lshl_add_u64 v[0:1], s[34:35], 0, v[144:145]
	v_mul_f32_e32 v2, 0x3b800000, v16
	v_add_f32_e32 v20, v20, v21
	flat_atomic_add_f32 v[0:1], v2
	v_mul_f32_e32 v2, 0x3b800000, v18
	v_add_f32_e32 v22, v22, v23
	flat_atomic_add_f32 v[0:1], v2 offset:4
	v_mul_f32_e32 v2, 0x3b800000, v20
	v_add_f32_e32 v24, v24, v25
	flat_atomic_add_f32 v[0:1], v2 offset:8
	v_mul_f32_e32 v2, 0x3b800000, v22
	v_add_f32_e32 v26, v26, v27
	flat_atomic_add_f32 v[0:1], v2 offset:12
	v_mul_f32_e32 v2, 0x3b800000, v24
	v_add_f32_e32 v28, v28, v29
	flat_atomic_add_f32 v[0:1], v2 offset:16
	v_mul_f32_e32 v2, 0x3b800000, v26
	v_add_f32_e32 v30, v30, v31
	flat_atomic_add_f32 v[0:1], v2 offset:20
	v_mul_f32_e32 v2, 0x3b800000, v28
	flat_atomic_add_f32 v[0:1], v2 offset:24
	v_mul_f32_e32 v2, 0x3b800000, v30
	flat_atomic_add_f32 v[0:1], v2 offset:28
